# combine+LayerNorm phases: wave reductions via DPP and v_permlane16/32_swap instead of six ds_bpermute round trips; LN+router phases: remaining xor16/32 steps via permlane swaps
# baseline (speedup 1.0000x reference)
; #define GAS __attribute__((address_space(1)))
; __device__ __forceinline__ const float* modp(const unsigned char* ws, int layer, int r, int chunk) { return (const float*)(ws + WS_MOD) + ((size_t)(layer * 3 + r) * 6 + chunk) * D; }
; __device__ __forceinline__ void phase_ln_router(const Frame& F, const Args& a, int layer) {
;     ...
;         for (int j = F.wave; j < TPB; j += 8) { const int row = rb + j; bf16_t* xr = X + (size_t)row * D;
;             f32x4 v[8]; float s = 0.f;
; #pragma unroll
;             for (int i = 0; i < 8; ++i) { const u32x2 p = *(const GAS u32x2*)(xr + 4 * F.lane + 256 * i); v[i] = (f32x4){bflo(p.x), bfhi(p.x), bflo(p.y), bfhi(p.y)}; s += (v[i][0] + v[i][1]) + (v[i][2] + v[i][3]); }
;             const int r = modrow(row);
;             if (r != rcur) { rcur = r; const float* sh2 = modp(F.ws, layer, r, 3); const float* sc2 = modp(F.ws, layer, r, 4);
; #pragma unroll
;                 for (int i = 0; i < 8; ++i) { const int c = 4 * F.lane + 256 * i; psc[i] = *(const GAS f32x4*)(sc2 + c) + 1.0f; psh[i] = *(const GAS f32x4*)(sh2 + c); } }
;             const float mean = wave_sum(s) * (1.0f / D); float ss = 0.f;
; #pragma unroll
;             for (int i = 0; i < 8; ++i) { v[i] = v[i] - mean; ss += (v[i][0] * v[i][0] + v[i][1] * v[i][1]) + (v[i][2] * v[i][2] + v[i][3] * v[i][3]); }
;             const float rstd = rsqrtf(wave_sum(ss) * (1.0f / D) + LN_EPS);
.LBB0_1290:
	s_waitcnt vmcnt(0)
	v_lshlrev_b32_e32 v92, 16, v86
	v_and_b32_e32 v93, 0xffff0000, v86
	v_lshlrev_b32_e32 v98, 16, v87
	v_and_b32_e32 v99, 0xffff0000, v87
	v_add_f32_e32 v86, v92, v93
	v_add_f32_e32 v87, v98, v99
	v_lshlrev_b32_e32 v100, 16, v84
	v_and_b32_e32 v101, 0xffff0000, v84
	v_lshlrev_b32_e32 v102, 16, v85
	v_and_b32_e32 v103, 0xffff0000, v85
	v_add_f32_e32 v86, v86, v87
	v_add_f32_e32 v84, v100, v101
	v_add_f32_e32 v85, v102, v103
	v_lshlrev_b32_e32 v104, 16, v82
	v_and_b32_e32 v105, 0xffff0000, v82
	v_lshlrev_b32_e32 v106, 16, v83
	v_and_b32_e32 v107, 0xffff0000, v83
	v_add_f32_e32 v86, 0, v86
	v_add_f32_e32 v84, v84, v85
	v_add_f32_e32 v82, v104, v105
	v_add_f32_e32 v83, v106, v107
	v_lshlrev_b32_e32 v94, 16, v80
	v_and_b32_e32 v95, 0xffff0000, v80
	v_lshlrev_b32_e32 v96, 16, v81
	v_and_b32_e32 v97, 0xffff0000, v81
	v_add_f32_e32 v84, v86, v84
	v_add_f32_e32 v82, v82, v83
	v_add_f32_e32 v80, v94, v95
	v_add_f32_e32 v81, v96, v97
	v_lshlrev_b32_e32 v86, 16, v76
	v_and_b32_e32 v87, 0xffff0000, v76
	v_lshlrev_b32_e32 v88, 16, v77
	v_and_b32_e32 v89, 0xffff0000, v77
	v_add_f32_e32 v82, v84, v82
	v_add_f32_e32 v80, v80, v81
	v_add_f32_e32 v76, v86, v87
	v_add_f32_e32 v77, v88, v89
	v_add_f32_e32 v80, v82, v80
	v_add_f32_e32 v76, v76, v77
	v_add_f32_e32 v76, v80, v76
	v_lshlrev_b32_e32 v80, 16, v72
	v_and_b32_e32 v81, 0xffff0000, v72
	v_lshlrev_b32_e32 v82, 16, v73
	v_and_b32_e32 v83, 0xffff0000, v73
	v_add_f32_e32 v72, v80, v81
	v_add_f32_e32 v73, v82, v83
	v_add_f32_e32 v72, v72, v73
	v_add_f32_e32 v76, v76, v72
	v_lshlrev_b32_e32 v72, 16, v74
	v_and_b32_e32 v73, 0xffff0000, v74
	v_lshlrev_b32_e32 v74, 16, v75
	v_and_b32_e32 v75, 0xffff0000, v75
	v_add_f32_e32 v77, v72, v73
	v_add_f32_e32 v84, v74, v75
	v_add_f32_e32 v77, v77, v84
	v_add_f32_e32 v84, v76, v77
	v_lshlrev_b32_e32 v76, 16, v78
	v_and_b32_e32 v77, 0xffff0000, v78
	v_lshlrev_b32_e32 v78, 16, v79
	v_and_b32_e32 v79, 0xffff0000, v79
	v_add_f32_e32 v85, v76, v77
	v_add_f32_e32 v90, v78, v79
	v_add_f32_e32 v85, v85, v90
	v_add_f32_e32 v84, v84, v85
	s_mov_b32 s0, 0x800000
	v_mov_b32_e32 v176, 0
	s_add_i32 s22, s30, 8
	s_cmp_gt_u32 s30, 25
	s_waitcnt lgkmcnt(0)
	s_nop 1
	v_add_f32_dpp v84, v84, v84 quad_perm:[1,0,3,2] row_mask:0xf bank_mask:0xf
	s_waitcnt lgkmcnt(0)
	s_nop 1
	v_add_f32_dpp v84, v84, v84 quad_perm:[2,3,0,1] row_mask:0xf bank_mask:0xf
	s_waitcnt lgkmcnt(0)
	s_nop 1
	v_add_f32_dpp v84, v84, v84 row_half_mirror row_mask:0xf bank_mask:0xf
	s_waitcnt lgkmcnt(0)
	s_nop 1
	v_add_f32_dpp v84, v84, v84 row_mirror row_mask:0xf bank_mask:0xf
	v_mov_b32_e32 v85, v84
	s_nop 1
	v_permlane16_swap_b32 v85, v84
	s_waitcnt lgkmcnt(0)
	v_add_f32_e32 v84, v84, v85
	v_mov_b32_e32 v85, v84
	s_nop 1
	v_permlane32_swap_b32 v85, v84
	s_waitcnt lgkmcnt(0)
	v_add_f32_e32 v90, v84, v85
	v_fmac_f32_e32 v93, 0xba000000, v90
	v_fmac_f32_e32 v101, 0xba000000, v90
	v_fmac_f32_e32 v99, 0xba000000, v90
	v_fmac_f32_e32 v92, 0xba000000, v90
	v_fmac_f32_e32 v103, 0xba000000, v90
	v_fmac_f32_e32 v100, 0xba000000, v90
	v_mov_b32_e32 v140, v93
	v_mov_b32_e32 v141, v101
	v_fmac_f32_e32 v98, 0xba000000, v90
	v_fmac_f32_e32 v102, 0xba000000, v90
	v_mov_b32_e32 v84, v92
	v_mov_b32_e32 v85, v100
	v_pk_mul_f32 v[140:141], v[140:141], v[140:141]
	v_mov_b32_e32 v164, v99
	v_mov_b32_e32 v165, v103
	v_pk_fma_f32 v[84:85], v[84:85], v[84:85], v[140:141]
	v_mov_b32_e32 v140, v98
	v_mov_b32_e32 v141, v102
	v_pk_mul_f32 v[164:165], v[164:165], v[164:165]
	v_fmac_f32_e32 v105, 0xba000000, v90
	v_pk_fma_f32 v[140:141], v[140:141], v[140:141], v[164:165]
	v_fmac_f32_e32 v104, 0xba000000, v90
	v_pk_add_f32 v[84:85], v[84:85], v[140:141]
	v_fmac_f32_e32 v107, 0xba000000, v90
	v_fmac_f32_e32 v106, 0xba000000, v90
	v_pk_add_f32 v[84:85], v[84:85], v[84:85] op_sel_hi:[0,1]
	v_pk_mul_f32 v[140:141], v[106:107], v[106:107]
	v_pk_mul_f32 v[164:165], v[104:105], v[104:105]
	v_fmac_f32_e32 v94, 0xba000000, v90
	v_pk_mov_b32 v[166:167], v[164:165], v[140:141] op_sel:[1,0]
	v_mov_b32_e32 v165, v141
	v_fmac_f32_e32 v95, 0xba000000, v90
	v_fmac_f32_e32 v96, 0xba000000, v90
	v_mul_f32_e32 v84, v94, v94
	v_pk_add_f32 v[140:141], v[166:167], v[164:165]
	v_fmac_f32_e32 v97, 0xba000000, v90
	v_pk_fma_f32 v[164:165], v[94:95], v[94:95], v[84:85] op_sel_hi:[1,1,0]
	v_mul_f32_e32 v84, v96, v96
	v_pk_add_f32 v[140:141], v[140:141], v[140:141] op_sel_hi:[0,1]
	v_pk_fma_f32 v[166:167], v[96:97], v[96:97], v[84:85] op_sel_hi:[1,1,0]
	v_fmac_f32_e32 v89, 0xba000000, v90
	v_fmac_f32_e32 v88, 0xba000000, v90
	v_fmac_f32_e32 v87, 0xba000000, v90
	v_fmac_f32_e32 v86, 0xba000000, v90
	v_mul_f32_e32 v164, v86, v86
	v_mul_f32_e32 v166, v87, v87
	v_mul_f32_e32 v140, v88, v88
	v_mul_f32_e32 v84, v89, v89
	v_pk_add_f32 v[164:165], v[164:165], v[166:167]
	v_pk_add_f32 v[84:85], v[140:141], v[84:85]
	v_fmac_f32_e32 v81, 0xba000000, v90
	v_pk_add_f32 v[84:85], v[164:165], v[84:85]
	v_fmac_f32_e32 v80, 0xba000000, v90
	v_fmac_f32_e32 v83, 0xba000000, v90
	v_fmac_f32_e32 v82, 0xba000000, v90
	v_pk_add_f32 v[84:85], v[84:85], v[84:85] op_sel_hi:[0,1]
	v_pk_mul_f32 v[140:141], v[82:83], v[82:83]
	v_pk_mul_f32 v[172:173], v[80:81], v[80:81]
	v_fmac_f32_e32 v72, 0xba000000, v90
	v_pk_mov_b32 v[174:175], v[172:173], v[140:141] op_sel:[1,0]
	v_mov_b32_e32 v173, v141
	v_fmac_f32_e32 v73, 0xba000000, v90
	v_fmac_f32_e32 v74, 0xba000000, v90
	v_mul_f32_e32 v84, v72, v72
	v_pk_add_f32 v[140:141], v[174:175], v[172:173]
	v_fmac_f32_e32 v75, 0xba000000, v90
	v_pk_fma_f32 v[172:173], v[72:73], v[72:73], v[84:85] op_sel_hi:[1,1,0]
	v_mul_f32_e32 v84, v74, v74
	v_pk_add_f32 v[140:141], v[140:141], v[140:141] op_sel_hi:[0,1]
	v_pk_fma_f32 v[174:175], v[74:75], v[74:75], v[84:85] op_sel_hi:[1,1,0]
	v_fmac_f32_e32 v79, 0xba000000, v90
	v_fmac_f32_e32 v78, 0xba000000, v90
	v_fmac_f32_e32 v77, 0xba000000, v90
	v_fmac_f32_e32 v76, 0xba000000, v90
	v_mul_f32_e32 v172, v76, v76
	v_mul_f32_e32 v174, v77, v77
	v_mul_f32_e32 v140, v78, v78
	v_mul_f32_e32 v84, v79, v79
	v_pk_add_f32 v[172:173], v[172:173], v[174:175]
	v_pk_add_f32 v[84:85], v[140:141], v[84:85]
	s_nop 0
	v_pk_add_f32 v[84:85], v[172:173], v[84:85]
	s_nop 0
	v_add_f32_e32 v84, v84, v85
	s_waitcnt lgkmcnt(0)
; #define GAS __attribute__((address_space(1)))
; #define LAS __attribute__((address_space(3)))
; __device__ __forceinline__ unsigned pk2(float lo, float hi) { return f2bf(lo) | (f2bf(hi) << 16); }
; __device__ __forceinline__ unsigned pk4_fp8(float a, float b, float c, float d) { int w = 0; w = __builtin_amdgcn_cvt_pk_fp8_f32(sat8(a), sat8(b), w, false); w = __builtin_amdgcn_cvt_pk_fp8_f32(sat8(c), sat8(d), w, true); return (unsigned)w; }
; __device__ __forceinline__ void phase_ln_router(const Frame& F, const Args& a, int layer) {
;     ...
;             const float rstd = rsqrtf(wave_sum(ss) * (1.0f / D) + LN_EPS);
; #pragma unroll
;             for (int i = 0; i < 8; ++i) { const int c = 4 * F.lane + 256 * i;
;                 const f32x4 lat = v[i] * rstd * *(const GAS f32x4*)(lng + c) + *(const GAS f32x4*)(lnb + c);
;                 { u32x2 wl; wl.x = pk2(lat[0], lat[1]); wl.y = pk2(lat[2], lat[3]); *(GAS u32x2*)(xr + c) = wl; }
;                 const f32x4 h = lat * psc[i] + psh[i];
;                 u32x2 w; w.x = pk2(h[0], h[1]); w.y = pk2(h[2], h[3]); *(GAS unsigned*)((unsigned char*)A0 + (size_t)row * D + c) = pk4_fp8(h[0], h[1], h[2], h[3]);
;                 *(LAS u32x2*)(hb + j * HB_LD + c) = w; } }
	s_nop 1
	v_add_f32_dpp v84, v84, v84 quad_perm:[1,0,3,2] row_mask:0xf bank_mask:0xf
	s_waitcnt lgkmcnt(0)
	s_nop 1
	v_add_f32_dpp v84, v84, v84 quad_perm:[2,3,0,1] row_mask:0xf bank_mask:0xf
	s_waitcnt lgkmcnt(0)
	s_nop 1
	v_add_f32_dpp v84, v84, v84 row_half_mirror row_mask:0xf bank_mask:0xf
	s_waitcnt lgkmcnt(0)
	s_nop 1
	v_add_f32_dpp v84, v84, v84 row_mirror row_mask:0xf bank_mask:0xf
	v_mov_b32_e32 v85, v84
	s_nop 1
	v_permlane16_swap_b32 v85, v84
	s_waitcnt lgkmcnt(0)
	v_add_f32_e32 v84, v84, v85
	v_mov_b32_e32 v85, v84
	s_nop 1
	v_permlane32_swap_b32 v85, v84
	s_waitcnt lgkmcnt(0)
	v_add_f32_e32 v84, v84, v85
	v_fmamk_f32 v84, v84, 0x3a000000, v155
	v_mul_f32_e32 v85, 0x4b800000, v84
	v_cmp_gt_f32_e32 vcc, s0, v84
	s_mov_b64 s[0:1], 0x34000000
	s_nop 0
	v_cndmask_b32_e32 v84, v84, v85, vcc
	v_rsq_f32_e32 v90, v84
	v_lshl_add_u64 v[84:85], v[70:71], 0, s[0:1]
	s_mov_b32 s0, 0x38400000
	v_mul_f32_e32 v140, 0x45800000, v90
	v_cndmask_b32_e32 v90, v90, v140, vcc
	v_pk_mul_f32 v[92:93], v[92:93], v[90:91] op_sel_hi:[1,0]
	v_pk_mul_f32 v[98:99], v[98:99], v[90:91] op_sel_hi:[1,0]
	v_pk_fma_f32 v[92:93], v[196:197], v[92:93], v[200:201]
	v_pk_fma_f32 v[98:99], v[198:199], v[98:99], v[202:203]
	v_bfe_u32 v140, v92, 16, 1
	v_add3_u32 v140, v92, v140, s39
	v_bfe_u32 v141, v93, 16, 1
	v_lshrrev_b32_e32 v140, 16, v140
	v_add3_u32 v141, v93, v141, s39
	v_and_or_b32 v140, v141, s38, v140
	v_bfe_u32 v141, v98, 16, 1
	v_add3_u32 v141, v98, v141, s39
	v_bfe_u32 v163, v99, 16, 1
	v_lshrrev_b32_e32 v141, 16, v141
	v_add3_u32 v163, v99, v163, s39
	v_and_or_b32 v141, v163, s38, v141
	v_pk_fma_f32 v[92:93], v[6:7], v[92:93], v[2:3]
	global_store_dwordx2 v[84:85], v[140:141], off
	v_med3_f32 v84, v92, s40, v160
	v_med3_f32 v85, v93, s40, v160
	v_mov_b32_e32 v140, 0
	v_cvt_pk_fp8_f32 v140, v84, v85
	v_pk_fma_f32 v[98:99], v[8:9], v[98:99], v[4:5]
	v_pk_mul_f32 v[100:101], v[100:101], v[90:91] op_sel_hi:[1,0]
	v_med3_f32 v84, v98, s40, v160
	v_med3_f32 v85, v99, s40, v160
	v_cvt_pk_fp8_f32 v140, v84, v85 op_sel:[0,0,1]
	v_lshl_add_u64 v[84:85], s[92:93], 0, v[66:67]
	v_add_co_u32_e32 v84, vcc, s0, v84
	v_pk_mul_f32 v[102:103], v[102:103], v[90:91] op_sel_hi:[1,0]
	s_nop 0
	v_addc_co_u32_e32 v85, vcc, 0, v85, vcc
	global_store_dword v[84:85], v140, off
	s_mov_b64 s[0:1], 0x34000200
	v_lshl_add_u64 v[140:141], v[70:71], 0, s[0:1]
	v_pk_mul_f32 v[104:105], v[104:105], v[90:91] op_sel_hi:[1,0]
	v_pk_mul_f32 v[106:107], v[106:107], v[90:91] op_sel_hi:[1,0]
	s_mov_b64 s[0:1], 0x34000400
	v_pk_mul_f32 v[94:95], v[94:95], v[90:91] op_sel_hi:[1,0]
	v_pk_mul_f32 v[96:97], v[96:97], v[90:91] op_sel_hi:[1,0]
	v_pk_mul_f32 v[86:87], v[86:87], v[90:91] op_sel_hi:[1,0]
	v_pk_mul_f32 v[88:89], v[88:89], v[90:91] op_sel_hi:[1,0]
	v_pk_mul_f32 v[80:81], v[80:81], v[90:91] op_sel_hi:[1,0]
	v_pk_mul_f32 v[82:83], v[82:83], v[90:91] op_sel_hi:[1,0]
	v_pk_mul_f32 v[72:73], v[72:73], v[90:91] op_sel_hi:[1,0]
	v_pk_mul_f32 v[74:75], v[74:75], v[90:91] op_sel_hi:[1,0]
	v_pk_mul_f32 v[172:173], v[76:77], v[90:91] op_sel_hi:[1,0]
	v_and_b32_sdwa v76, v98, v159 dst_sel:DWORD dst_unused:UNUSED_PAD src0_sel:WORD_1 src1_sel:DWORD
	v_and_b32_sdwa v77, v92, v159 dst_sel:DWORD dst_unused:UNUSED_PAD src0_sel:WORD_1 src1_sel:DWORD
	v_pk_mul_f32 v[174:175], v[78:79], v[90:91] op_sel_hi:[1,0]
	v_add3_u32 v90, v92, v77, s39
	v_add3_u32 v92, v98, v76, s39
	v_and_b32_sdwa v78, v99, v159 dst_sel:DWORD dst_unused:UNUSED_PAD src0_sel:WORD_1 src1_sel:DWORD
	v_add3_u32 v98, v99, v78, s39
	v_and_b32_sdwa v79, v93, v159 dst_sel:DWORD dst_unused:UNUSED_PAD src0_sel:WORD_1 src1_sel:DWORD
	v_add3_u32 v93, v93, v79, s39
	v_and_b32_e32 v98, 0xffff0000, v98
	v_and_b32_e32 v99, 0xffff0000, v93
	v_or_b32_sdwa v93, v98, v92 dst_sel:DWORD dst_unused:UNUSED_PAD src0_sel:DWORD src1_sel:WORD_1
	v_or_b32_sdwa v92, v99, v90 dst_sel:DWORD dst_unused:UNUSED_PAD src0_sel:DWORD src1_sel:WORD_1
	v_pk_fma_f32 v[100:101], v[204:205], v[100:101], v[208:209]
	v_pk_fma_f32 v[166:167], v[206:207], v[102:103], v[210:211]
	v_bfe_u32 v102, v100, 16, 1
	v_add3_u32 v102, v100, v102, s39
	v_bfe_u32 v103, v101, 16, 1
	v_lshrrev_b32_e32 v102, 16, v102
	v_add3_u32 v103, v101, v103, s39
	v_and_or_b32 v164, v103, s38, v102
	v_bfe_u32 v102, v166, 16, 1
	v_add3_u32 v102, v166, v102, s39
	v_pk_fma_f32 v[100:101], v[14:15], v[100:101], v[10:11]
	v_lshrrev_b32_e32 v163, 16, v102
	v_med3_f32 v102, v100, s40, v160
	v_med3_f32 v103, v101, s40, v160
	v_mov_b32_e32 v168, 0
	v_cvt_pk_fp8_f32 v168, v102, v103
	v_pk_fma_f32 v[102:103], v[16:17], v[166:167], v[12:13]
	v_bfe_u32 v165, v167, 16, 1
	v_med3_f32 v166, v102, s40, v160
	v_med3_f32 v169, v103, s40, v160
	v_cvt_pk_fp8_f32 v168, v166, v169 op_sel:[0,0,1]
	v_add3_u32 v165, v167, v165, s39
	v_and_or_b32 v165, v165, s38, v163
	global_store_dwordx2 v[140:141], v[164:165], off
	global_store_dword v[84:85], v168, off offset:256
	v_mov_b32_e32 v163, 0
	v_lshl_add_u64 v[140:141], v[70:71], 0, s[0:1]
	s_mov_b64 s[0:1], 0x34000600
	v_and_b32_sdwa v98, v100, v159 dst_sel:DWORD dst_unused:UNUSED_PAD src0_sel:WORD_1 src1_sel:DWORD
	v_and_b32_sdwa v99, v103, v159 dst_sel:DWORD dst_unused:UNUSED_PAD src0_sel:WORD_1 src1_sel:DWORD
	v_and_b32_sdwa v90, v102, v159 dst_sel:DWORD dst_unused:UNUSED_PAD src0_sel:WORD_1 src1_sel:DWORD
	v_add3_u32 v98, v100, v98, s39
	v_add3_u32 v99, v103, v99, s39
	v_add3_u32 v90, v102, v90, s39
	v_and_b32_e32 v99, 0xffff0000, v99
	v_or_b32_sdwa v99, v99, v90 dst_sel:DWORD dst_unused:UNUSED_PAD src0_sel:DWORD src1_sel:WORD_1
	v_pk_fma_f32 v[164:165], v[214:215], v[104:105], v[218:219]
	v_pk_fma_f32 v[166:167], v[216:217], v[106:107], v[220:221]
	v_bfe_u32 v168, v164, 16, 1
; #define GAS __attribute__((address_space(1)))
; #define LAS __attribute__((address_space(3)))
; __device__ __forceinline__ unsigned pk2(float lo, float hi) { return f2bf(lo) | (f2bf(hi) << 16); }
; __device__ __forceinline__ unsigned pk4_fp8(float a, float b, float c, float d) { int w = 0; w = __builtin_amdgcn_cvt_pk_fp8_f32(sat8(a), sat8(b), w, false); w = __builtin_amdgcn_cvt_pk_fp8_f32(sat8(c), sat8(d), w, true); return (unsigned)w; }
; __device__ __forceinline__ void phase_ln_router(const Frame& F, const Args& a, int layer) {
;     ...
;             for (int i = 0; i < 8; ++i) { const int c = 4 * F.lane + 256 * i;
;                 const f32x4 lat = v[i] * rstd * *(const GAS f32x4*)(lng + c) + *(const GAS f32x4*)(lnb + c);
;                 { u32x2 wl; wl.x = pk2(lat[0], lat[1]); wl.y = pk2(lat[2], lat[3]); *(GAS u32x2*)(xr + c) = wl; }
;                 const f32x4 h = lat * psc[i] + psh[i];
;                 u32x2 w; w.x = pk2(h[0], h[1]); w.y = pk2(h[2], h[3]); *(GAS unsigned*)((unsigned char*)A0 + (size_t)row * D + c) = pk4_fp8(h[0], h[1], h[2], h[3]);
;                 *(LAS u32x2*)(hb + j * HB_LD + c) = w; } }
	v_bfe_u32 v169, v165, 16, 1
	v_pk_fma_f32 v[106:107], v[22:23], v[164:165], v[18:19]
	v_add3_u32 v164, v164, v168, s39
	v_add3_u32 v165, v165, v169, s39
	v_med3_f32 v168, v106, s40, v160
	v_med3_f32 v169, v107, s40, v160
	v_cvt_pk_fp8_f32 v163, v168, v169
	v_bfe_u32 v170, v166, 16, 1
	v_pk_fma_f32 v[104:105], v[24:25], v[166:167], v[20:21]
	v_add3_u32 v166, v166, v170, s39
	v_med3_f32 v170, v104, s40, v160
	v_med3_f32 v168, v105, s40, v160
	v_bfe_u32 v171, v167, 16, 1
	v_cvt_pk_fp8_f32 v163, v170, v168 op_sel:[0,0,1]
	v_add3_u32 v167, v167, v171, s39
	v_lshrrev_b32_e32 v164, 16, v164
	v_lshrrev_b32_e32 v166, 16, v166
	v_and_or_b32 v164, v165, s38, v164
	v_and_or_b32 v165, v167, s38, v166
	global_store_dwordx2 v[140:141], v[164:165], off
	global_store_dword v[84:85], v163, off offset:512
	v_mov_b32_e32 v163, 0
	v_lshl_add_u64 v[140:141], v[70:71], 0, s[0:1]
	s_mov_b64 s[0:1], 0x34000800
	v_and_b32_sdwa v90, v104, v159 dst_sel:DWORD dst_unused:UNUSED_PAD src0_sel:WORD_1 src1_sel:DWORD
	v_add3_u32 v90, v104, v90, s39
	v_pk_fma_f32 v[164:165], v[222:223], v[94:95], v[226:227]
	v_pk_fma_f32 v[166:167], v[224:225], v[96:97], v[228:229]
	v_bfe_u32 v168, v164, 16, 1
	v_bfe_u32 v169, v165, 16, 1
	v_pk_fma_f32 v[96:97], v[30:31], v[164:165], v[26:27]
	v_add3_u32 v164, v164, v168, s39
	v_add3_u32 v165, v165, v169, s39
	v_med3_f32 v168, v96, s40, v160
	v_med3_f32 v169, v97, s40, v160
	v_cvt_pk_fp8_f32 v163, v168, v169
	v_bfe_u32 v170, v166, 16, 1
	v_pk_fma_f32 v[94:95], v[32:33], v[166:167], v[28:29]
	v_add3_u32 v166, v166, v170, s39
	v_med3_f32 v170, v94, s40, v160
	v_med3_f32 v168, v95, s40, v160
	v_bfe_u32 v171, v167, 16, 1
	v_cvt_pk_fp8_f32 v163, v170, v168 op_sel:[0,0,1]
	v_add3_u32 v167, v167, v171, s39
	v_lshrrev_b32_e32 v164, 16, v164
	v_lshrrev_b32_e32 v166, 16, v166
	v_and_or_b32 v164, v165, s38, v164
	v_and_or_b32 v165, v167, s38, v166
	global_store_dwordx2 v[140:141], v[164:165], off
	global_store_dword v[84:85], v163, off offset:768
	v_mov_b32_e32 v163, 0
	v_lshl_add_u64 v[140:141], v[70:71], 0, s[0:1]
	s_mov_b64 s[0:1], 0x34000a00
	v_pk_fma_f32 v[164:165], v[86:87], v[230:231], v[234:235]
	v_pk_fma_f32 v[166:167], v[88:89], v[232:233], v[236:237]
	v_bfe_u32 v168, v164, 16, 1
	v_bfe_u32 v169, v165, 16, 1
	v_pk_fma_f32 v[88:89], v[38:39], v[164:165], v[34:35]
	v_add3_u32 v164, v164, v168, s39
	v_add3_u32 v165, v165, v169, s39
	v_med3_f32 v168, v88, s40, v160
	v_med3_f32 v169, v89, s40, v160
	v_cvt_pk_fp8_f32 v163, v168, v169
	v_bfe_u32 v170, v166, 16, 1
	v_pk_fma_f32 v[86:87], v[40:41], v[166:167], v[36:37]
	v_add3_u32 v166, v166, v170, s39
	v_med3_f32 v170, v86, s40, v160
	v_med3_f32 v168, v87, s40, v160
	v_bfe_u32 v171, v167, 16, 1
	v_cvt_pk_fp8_f32 v163, v170, v168 op_sel:[0,0,1]
	v_add3_u32 v167, v167, v171, s39
	v_lshrrev_b32_e32 v164, 16, v164
	v_lshrrev_b32_e32 v166, 16, v166
	v_and_or_b32 v164, v165, s38, v164
	v_and_or_b32 v165, v167, s38, v166
	global_store_dwordx2 v[140:141], v[164:165], off
	global_store_dword v[84:85], v163, off offset:1024
	v_mov_b32_e32 v163, 0
	v_lshl_add_u64 v[140:141], v[70:71], 0, s[0:1]
	s_mov_b64 s[0:1], 0x34000c00
	v_pk_fma_f32 v[80:81], v[80:81], v[238:239], v[118:119]
	v_pk_fma_f32 v[82:83], v[82:83], v[240:241], v[120:121]
	v_bfe_u32 v164, v80, 16, 1
	v_bfe_u32 v165, v81, 16, 1
	v_pk_fma_f32 v[170:171], v[46:47], v[80:81], v[42:43]
	v_add3_u32 v80, v80, v164, s39
	v_add3_u32 v81, v81, v165, s39
	v_med3_f32 v164, v170, s40, v160
	v_med3_f32 v165, v171, s40, v160
	v_cvt_pk_fp8_f32 v163, v164, v165
	v_bfe_u32 v166, v82, 16, 1
	v_pk_fma_f32 v[168:169], v[48:49], v[82:83], v[44:45]
	v_add3_u32 v82, v82, v166, s39
	v_med3_f32 v166, v168, s40, v160
	v_med3_f32 v164, v169, s40, v160
	v_bfe_u32 v167, v83, 16, 1
	v_cvt_pk_fp8_f32 v163, v166, v164 op_sel:[0,0,1]
	v_add3_u32 v83, v83, v167, s39
	v_lshrrev_b32_e32 v80, 16, v80
	v_lshrrev_b32_e32 v82, 16, v82
	v_and_or_b32 v80, v81, s38, v80
	v_and_or_b32 v81, v83, s38, v82
	global_store_dwordx2 v[140:141], v[80:81], off
	global_store_dword v[84:85], v163, off offset:1280
	v_mov_b32_e32 v163, 0
	v_lshl_add_u64 v[140:141], v[70:71], 0, s[0:1]
	s_mov_b64 s[0:1], 0x34000e00
	v_lshl_add_u64 v[70:71], v[70:71], 0, s[0:1]
	s_mov_b64 s[0:1], 0x4000
	v_lshl_add_u64 v[66:67], v[66:67], 0, s[0:1]
	s_mov_b64 s[0:1], 0x8000
	v_lshl_add_u64 v[68:69], v[68:69], 0, s[0:1]
	v_pk_fma_f32 v[72:73], v[72:73], v[242:243], v[122:123]
	v_pk_fma_f32 v[74:75], v[74:75], v[244:245], v[124:125]
	v_bfe_u32 v76, v72, 16, 1
	v_bfe_u32 v77, v73, 16, 1
	v_pk_fma_f32 v[82:83], v[54:55], v[72:73], v[50:51]
	v_add3_u32 v72, v72, v76, s39
	v_add3_u32 v73, v73, v77, s39
	v_med3_f32 v76, v82, s40, v160
	v_med3_f32 v77, v83, s40, v160
	v_cvt_pk_fp8_f32 v163, v76, v77
	v_bfe_u32 v78, v74, 16, 1
	v_pk_fma_f32 v[80:81], v[56:57], v[74:75], v[52:53]
	v_add3_u32 v74, v74, v78, s39
	v_med3_f32 v78, v80, s40, v160
	v_med3_f32 v76, v81, s40, v160
	v_bfe_u32 v79, v75, 16, 1
	v_cvt_pk_fp8_f32 v163, v78, v76 op_sel:[0,0,1]
	v_add3_u32 v75, v75, v79, s39
	v_lshrrev_b32_e32 v72, 16, v72
	v_lshrrev_b32_e32 v74, 16, v74
	v_and_or_b32 v72, v73, s38, v72
	v_and_or_b32 v73, v75, s38, v74
	global_store_dwordx2 v[140:141], v[72:73], off
	global_store_dword v[84:85], v163, off offset:1536
	v_and_b32_sdwa v140, v101, v159 dst_sel:DWORD dst_unused:UNUSED_PAD src0_sel:WORD_1 src1_sel:DWORD
	v_add3_u32 v100, v101, v140, s39
	v_and_b32_e32 v100, 0xffff0000, v100
	v_or_b32_sdwa v98, v100, v98 dst_sel:DWORD dst_unused:UNUSED_PAD src0_sel:DWORD src1_sel:WORD_1
	ds_write2st64_b64 v113, v[92:93], v[98:99] offset1:1
	v_and_b32_sdwa v93, v105, v159 dst_sel:DWORD dst_unused:UNUSED_PAD src0_sel:WORD_1 src1_sel:DWORD
; #define GAS __attribute__((address_space(1)))
; #define LAS __attribute__((address_space(3)))
; __device__ __forceinline__ unsigned pk2(float lo, float hi) { return f2bf(lo) | (f2bf(hi) << 16); }
; __device__ __forceinline__ unsigned pk4_fp8(float a, float b, float c, float d) { int w = 0; w = __builtin_amdgcn_cvt_pk_fp8_f32(sat8(a), sat8(b), w, false); w = __builtin_amdgcn_cvt_pk_fp8_f32(sat8(c), sat8(d), w, true); return (unsigned)w; }
; __device__ __forceinline__ void phase_ln_router(const Frame& F, const Args& a, int layer) {
;     ...
;             for (int i = 0; i < 8; ++i) { const int c = 4 * F.lane + 256 * i;
;                 const f32x4 lat = v[i] * rstd * *(const GAS f32x4*)(lng + c) + *(const GAS f32x4*)(lnb + c);
;                 { u32x2 wl; wl.x = pk2(lat[0], lat[1]); wl.y = pk2(lat[2], lat[3]); *(GAS u32x2*)(xr + c) = wl; }
;                 const f32x4 h = lat * psc[i] + psh[i];
;                 u32x2 w; w.x = pk2(h[0], h[1]); w.y = pk2(h[2], h[3]); *(GAS unsigned*)((unsigned char*)A0 + (size_t)row * D + c) = pk4_fp8(h[0], h[1], h[2], h[3]);
;                 *(LAS u32x2*)(hb + j * HB_LD + c) = w; } }
	v_and_b32_sdwa v98, v107, v159 dst_sel:DWORD dst_unused:UNUSED_PAD src0_sel:WORD_1 src1_sel:DWORD
	v_add3_u32 v93, v105, v93, s39
	v_and_b32_sdwa v92, v106, v159 dst_sel:DWORD dst_unused:UNUSED_PAD src0_sel:WORD_1 src1_sel:DWORD
	v_add3_u32 v98, v107, v98, s39
	v_and_b32_e32 v93, 0xffff0000, v93
	v_add3_u32 v92, v106, v92, s39
	v_and_b32_e32 v98, 0xffff0000, v98
	v_or_b32_sdwa v93, v93, v90 dst_sel:DWORD dst_unused:UNUSED_PAD src0_sel:DWORD src1_sel:WORD_1
	v_and_b32_sdwa v90, v94, v159 dst_sel:DWORD dst_unused:UNUSED_PAD src0_sel:WORD_1 src1_sel:DWORD
	v_and_b32_sdwa v99, v95, v159 dst_sel:DWORD dst_unused:UNUSED_PAD src0_sel:WORD_1 src1_sel:DWORD
	v_and_b32_sdwa v100, v97, v159 dst_sel:DWORD dst_unused:UNUSED_PAD src0_sel:WORD_1 src1_sel:DWORD
	v_or_b32_sdwa v92, v98, v92 dst_sel:DWORD dst_unused:UNUSED_PAD src0_sel:DWORD src1_sel:WORD_1
	v_and_b32_sdwa v98, v96, v159 dst_sel:DWORD dst_unused:UNUSED_PAD src0_sel:WORD_1 src1_sel:DWORD
	v_add3_u32 v90, v94, v90, s39
	v_add3_u32 v94, v95, v99, s39
	v_add3_u32 v95, v97, v100, s39
	v_add3_u32 v96, v96, v98, s39
	v_and_b32_e32 v94, 0xffff0000, v94
	v_and_b32_e32 v97, 0xffff0000, v95
	v_or_b32_sdwa v95, v94, v90 dst_sel:DWORD dst_unused:UNUSED_PAD src0_sel:DWORD src1_sel:WORD_1
	v_or_b32_sdwa v94, v97, v96 dst_sel:DWORD dst_unused:UNUSED_PAD src0_sel:DWORD src1_sel:WORD_1
	ds_write2st64_b64 v113, v[92:93], v[94:95] offset0:2 offset1:3
	v_and_b32_sdwa v93, v87, v159 dst_sel:DWORD dst_unused:UNUSED_PAD src0_sel:WORD_1 src1_sel:DWORD
	v_and_b32_sdwa v94, v89, v159 dst_sel:DWORD dst_unused:UNUSED_PAD src0_sel:WORD_1 src1_sel:DWORD
	v_and_b32_sdwa v90, v86, v159 dst_sel:DWORD dst_unused:UNUSED_PAD src0_sel:WORD_1 src1_sel:DWORD
	v_and_b32_sdwa v92, v88, v159 dst_sel:DWORD dst_unused:UNUSED_PAD src0_sel:WORD_1 src1_sel:DWORD
	v_add3_u32 v87, v87, v93, s39
	v_add3_u32 v89, v89, v94, s39
	v_add3_u32 v88, v88, v92, s39
	v_add3_u32 v86, v86, v90, s39
	v_and_b32_e32 v87, 0xffff0000, v87
	v_and_b32_e32 v89, 0xffff0000, v89
	v_or_b32_sdwa v87, v87, v86 dst_sel:DWORD dst_unused:UNUSED_PAD src0_sel:DWORD src1_sel:WORD_1
	v_or_b32_sdwa v86, v89, v88 dst_sel:DWORD dst_unused:UNUSED_PAD src0_sel:DWORD src1_sel:WORD_1
	v_and_b32_sdwa v89, v170, v159 dst_sel:DWORD dst_unused:UNUSED_PAD src0_sel:WORD_1 src1_sel:DWORD
	v_and_b32_sdwa v90, v169, v159 dst_sel:DWORD dst_unused:UNUSED_PAD src0_sel:WORD_1 src1_sel:DWORD
	v_and_b32_sdwa v92, v171, v159 dst_sel:DWORD dst_unused:UNUSED_PAD src0_sel:WORD_1 src1_sel:DWORD
	v_and_b32_sdwa v88, v168, v159 dst_sel:DWORD dst_unused:UNUSED_PAD src0_sel:WORD_1 src1_sel:DWORD
	v_add3_u32 v93, v170, v89, s39
	v_add3_u32 v89, v169, v90, s39
	v_add3_u32 v90, v171, v92, s39
	v_add3_u32 v88, v168, v88, s39
	v_and_b32_e32 v89, 0xffff0000, v89
	v_and_b32_e32 v90, 0xffff0000, v90
	v_or_b32_sdwa v89, v89, v88 dst_sel:DWORD dst_unused:UNUSED_PAD src0_sel:DWORD src1_sel:WORD_1
	v_or_b32_sdwa v88, v90, v93 dst_sel:DWORD dst_unused:UNUSED_PAD src0_sel:DWORD src1_sel:WORD_1
	ds_write2st64_b64 v113, v[86:87], v[88:89] offset0:4 offset1:5
	v_and_b32_sdwa v88, v81, v159 dst_sel:DWORD dst_unused:UNUSED_PAD src0_sel:WORD_1 src1_sel:DWORD
	v_and_b32_sdwa v89, v83, v159 dst_sel:DWORD dst_unused:UNUSED_PAD src0_sel:WORD_1 src1_sel:DWORD
	v_add3_u32 v81, v81, v88, s39
	v_add3_u32 v83, v83, v89, s39
	v_and_b32_sdwa v86, v80, v159 dst_sel:DWORD dst_unused:UNUSED_PAD src0_sel:WORD_1 src1_sel:DWORD
	v_and_b32_sdwa v87, v82, v159 dst_sel:DWORD dst_unused:UNUSED_PAD src0_sel:WORD_1 src1_sel:DWORD
	v_add3_u32 v82, v82, v87, s39
	v_add3_u32 v80, v80, v86, s39
	v_and_b32_e32 v81, 0xffff0000, v81
	v_and_b32_e32 v83, 0xffff0000, v83
	v_or_b32_sdwa v81, v81, v80 dst_sel:DWORD dst_unused:UNUSED_PAD src0_sel:DWORD src1_sel:WORD_1
	v_or_b32_sdwa v80, v83, v82 dst_sel:DWORD dst_unused:UNUSED_PAD src0_sel:DWORD src1_sel:WORD_1
	v_pk_fma_f32 v[72:73], v[172:173], v[250:251], v[126:127]
	v_pk_fma_f32 v[74:75], v[174:175], v[252:253], v[128:129]
	v_pk_fma_f32 v[78:79], v[58:59], v[72:73], v[62:63]
	v_bfe_u32 v82, v72, 16, 1
	v_med3_f32 v88, v78, s40, v160
	v_med3_f32 v89, v79, s40, v160
	v_cvt_pk_fp8_f32 v176, v88, v89
	v_bfe_u32 v86, v74, 16, 1
	v_bfe_u32 v87, v75, 16, 1
	v_pk_fma_f32 v[76:77], v[60:61], v[74:75], v[64:65]
	v_bfe_u32 v83, v73, 16, 1
	v_add3_u32 v72, v72, v82, s39
	v_add3_u32 v74, v74, v86, s39
	v_add3_u32 v75, v75, v87, s39
	v_and_b32_sdwa v86, v77, v159 dst_sel:DWORD dst_unused:UNUSED_PAD src0_sel:WORD_1 src1_sel:DWORD
	v_and_b32_sdwa v87, v79, v159 dst_sel:DWORD dst_unused:UNUSED_PAD src0_sel:WORD_1 src1_sel:DWORD
	v_med3_f32 v90, v76, s40, v160
	v_med3_f32 v92, v77, s40, v160
	v_add3_u32 v73, v73, v83, s39
	v_and_b32_sdwa v82, v76, v159 dst_sel:DWORD dst_unused:UNUSED_PAD src0_sel:WORD_1 src1_sel:DWORD
	v_and_b32_sdwa v83, v78, v159 dst_sel:DWORD dst_unused:UNUSED_PAD src0_sel:WORD_1 src1_sel:DWORD
	v_lshrrev_b32_e32 v72, 16, v72
	v_lshrrev_b32_e32 v74, 16, v74
	v_add3_u32 v77, v77, v86, s39
	v_add3_u32 v79, v79, v87, s39
	v_cvt_pk_fp8_f32 v176, v90, v92 op_sel:[0,0,1]
	v_add3_u32 v78, v78, v83, s39
	v_add3_u32 v76, v76, v82, s39
	v_and_or_b32 v72, v73, s38, v72
	v_and_or_b32 v73, v75, s38, v74
	v_and_b32_e32 v74, 0xffff0000, v77
	v_and_b32_e32 v75, 0xffff0000, v79
	global_store_dwordx2 v[70:71], v[72:73], off
	v_or_b32_sdwa v71, v74, v76 dst_sel:DWORD dst_unused:UNUSED_PAD src0_sel:DWORD src1_sel:WORD_1
	v_or_b32_sdwa v70, v75, v78 dst_sel:DWORD dst_unused:UNUSED_PAD src0_sel:DWORD src1_sel:WORD_1
	ds_write2st64_b64 v113, v[80:81], v[70:71] offset0:6 offset1:7
	v_add_u32_e32 v113, 0x8080, v113
	global_store_dword v[84:85], v176, off offset:1792
	s_cbranch_scc1 .LBB0_1292
	s_mov_b32 s30, s22
	s_branch .LBB0_1288

; __device__ __forceinline__ void phase_ln_router(const Frame& F, const Args& a, int layer) {
;     ...
;             const bool sel = gsel && rank < TOPK;
;             const float wsum = wave_sum(sel ? sg : 0.f);
;             if (sel) { SE[row * 8 + rank] = F.lane; SW[row * 8 + rank] = sg / wsum * 2.5f; mycnt += 1; } }
.LBB0_1330:
	v_cmp_gt_u32_e64 s[0:1], 8, v74
	s_and_b64 vcc, vcc, s[0:1]
	v_cndmask_b32_e32 v75, 0, v73, vcc
	s_waitcnt lgkmcnt(0)
	s_nop 1
	v_add_f32_dpp v75, v75, v75 quad_perm:[1,0,3,2] row_mask:0xf bank_mask:0xf
	s_waitcnt lgkmcnt(0)
	s_nop 1
	v_add_f32_dpp v75, v75, v75 quad_perm:[2,3,0,1] row_mask:0xf bank_mask:0xf
	s_waitcnt lgkmcnt(0)
	s_nop 1
	v_add_f32_dpp v75, v75, v75 row_half_mirror row_mask:0xf bank_mask:0xf
	s_waitcnt lgkmcnt(0)
	s_nop 1
	v_add_f32_dpp v75, v75, v75 row_mirror row_mask:0xf bank_mask:0xf
	v_mov_b32_e32 v76, v75
	s_nop 1
	v_permlane16_swap_b32 v76, v75
	s_waitcnt lgkmcnt(0)
	v_add_f32_e32 v75, v75, v76
	v_mov_b32_e32 v76, v75
	s_nop 1
	v_permlane32_swap_b32 v76, v75
	s_and_saveexec_b64 s[0:1], vcc
	s_cbranch_execz .LBB0_1332
	s_mul_i32 s22, s51, 34
	s_waitcnt lgkmcnt(0)
	v_add_f32_e32 v78, v75, v76
	s_add_i32 s22, s2, s22
	v_div_scale_f32 v79, s[28:29], v78, v78, v73
	v_lshl_or_b32 v74, s22, 3, v74
	v_rcp_f32_e32 v80, v79
	v_ashrrev_i32_e32 v75, 31, v74
	v_lshlrev_b64 v[74:75], 2, v[74:75]
	v_lshl_add_u64 v[76:77], s[24:25], 0, v[74:75]
	global_store_dword v[76:77], v1, off
	v_fma_f32 v76, -v79, v80, 1.0
	v_fmac_f32_e32 v80, v76, v80
	v_div_scale_f32 v76, vcc, v73, v78, v73
	v_mul_f32_e32 v77, v76, v80
	v_fma_f32 v81, -v79, v77, v76
	v_fmac_f32_e32 v77, v81, v80
	v_fma_f32 v76, -v79, v77, v76
	v_div_fmas_f32 v76, v76, v80, v77
	v_div_fixup_f32 v73, v76, v78, v73
	v_mul_f32_e32 v73, 0x40200000, v73
	v_lshl_add_u64 v[74:75], s[26:27], 0, v[74:75]
	v_add_u32_e32 v66, 1, v66
	global_store_dword v[74:75], v73, off

; #define GAS __attribute__((address_space(1)))
; __device__ __forceinline__ f32x4 up4_fp8(unsigned w) { const f32x2 lo = __builtin_amdgcn_cvt_pk_f32_fp8((int)w, false), hi = __builtin_amdgcn_cvt_pk_f32_fp8((int)w, true); return (f32x4){lo[0], lo[1], hi[0], hi[1]}; }
; __device__ __forceinline__ void phase_combine(const Frame& F, const Args& a, int layer) {
;     ...
;             for (int jj = 0; jj < 8; ++jj) { const int slot = TOK_SLOT[row * 8 + jj]; const float w = SW[row * 8 + jj] * 0.0625f; const unsigned char* ys = YS + (size_t)slot * D;
; #pragma unroll
;                 for (int i = 0; i < 8; ++i) f[i] += up4_fp8(*(const GAS unsigned*)(ys + 4 * F.lane + 256 * i)) * w; }
.LBB0_2391:
	s_add_i32 s26, s23, s10
	s_ashr_i32 s27, s26, 31
	s_lshl_b64 s[26:27], s[26:27], 2
	s_add_u32 s28, s9, s26
	s_addc_u32 s29, s14, s27
	global_load_dwordx2 v[74:75], v67, s[28:29]
	s_add_u32 s26, s2, s26
	s_addc_u32 s27, s7, s27
	global_load_dwordx2 v[108:109], v67, s[26:27]
	s_add_i32 s10, s10, 2
	s_cmp_eq_u32 s10, 8
	s_waitcnt vmcnt(1)
	v_ashrrev_i32_e32 v111, 31, v74
	v_mov_b32_e32 v110, v74
	v_ashrrev_i32_e32 v131, 31, v75
	v_mov_b32_e32 v130, v75
	v_lshlrev_b64 v[74:75], 11, v[110:111]
	v_lshlrev_b64 v[110:111], 11, v[130:131]
	v_lshl_add_u64 v[74:75], v[68:69], 0, v[74:75]
	v_lshl_add_u64 v[110:111], v[68:69], 0, v[110:111]
	global_load_dword v130, v[74:75], off
	global_load_dword v132, v[74:75], off offset:256
	global_load_dword v136, v[74:75], off offset:512
	global_load_dword v140, v[74:75], off offset:768
	global_load_dword v144, v[74:75], off offset:1024
	global_load_dword v148, v[74:75], off offset:1280
	global_load_dword v152, v[74:75], off offset:1536
	s_nop 0
	global_load_dword v75, v[74:75], off offset:1792
	s_nop 0
	global_load_dword v160, v[110:111], off
	global_load_dword v164, v[110:111], off offset:256
	global_load_dword v168, v[110:111], off offset:512
	global_load_dword v172, v[110:111], off offset:768
	global_load_dword v176, v[110:111], off offset:1024
	global_load_dword v180, v[110:111], off offset:1280
	global_load_dword v184, v[110:111], off offset:1536
	global_load_dword v188, v[110:111], off offset:1792
	s_waitcnt vmcnt(16)
	v_mul_f32_e32 v66, 0x3d800000, v108
	v_mul_f32_e32 v74, 0x3d800000, v109
	s_waitcnt vmcnt(15)
	v_cvt_pk_f32_fp8_e32 v[108:109], v130
	v_cvt_pk_f32_fp8_sdwa v[110:111], v130 src0_sel:WORD_1
	s_waitcnt vmcnt(14)
	v_cvt_pk_f32_fp8_e32 v[130:131], v132
	v_cvt_pk_f32_fp8_sdwa v[132:133], v132 src0_sel:WORD_1
	s_waitcnt vmcnt(13)
	v_cvt_pk_f32_fp8_e32 v[134:135], v136
	v_cvt_pk_f32_fp8_sdwa v[136:137], v136 src0_sel:WORD_1
	s_waitcnt vmcnt(12)
	v_cvt_pk_f32_fp8_e32 v[138:139], v140
	v_cvt_pk_f32_fp8_sdwa v[140:141], v140 src0_sel:WORD_1
	s_waitcnt vmcnt(11)
	v_cvt_pk_f32_fp8_e32 v[142:143], v144
	v_cvt_pk_f32_fp8_sdwa v[144:145], v144 src0_sel:WORD_1
	s_waitcnt vmcnt(10)
	v_cvt_pk_f32_fp8_e32 v[146:147], v148
	v_cvt_pk_f32_fp8_sdwa v[148:149], v148 src0_sel:WORD_1
	s_waitcnt vmcnt(9)
	v_cvt_pk_f32_fp8_e32 v[150:151], v152
	v_cvt_pk_f32_fp8_sdwa v[152:153], v152 src0_sel:WORD_1
	s_waitcnt vmcnt(8)
	v_cvt_pk_f32_fp8_e32 v[154:155], v75
	v_cvt_pk_f32_fp8_sdwa v[156:157], v75 src0_sel:WORD_1
	s_waitcnt vmcnt(7)
	v_cvt_pk_f32_fp8_e32 v[158:159], v160
	v_cvt_pk_f32_fp8_sdwa v[160:161], v160 src0_sel:WORD_1
	s_waitcnt vmcnt(6)
	v_cvt_pk_f32_fp8_e32 v[162:163], v164
	v_cvt_pk_f32_fp8_sdwa v[164:165], v164 src0_sel:WORD_1
	s_waitcnt vmcnt(5)
	v_cvt_pk_f32_fp8_e32 v[166:167], v168
	v_cvt_pk_f32_fp8_sdwa v[168:169], v168 src0_sel:WORD_1
	s_waitcnt vmcnt(4)
	v_cvt_pk_f32_fp8_e32 v[170:171], v172
	v_cvt_pk_f32_fp8_sdwa v[172:173], v172 src0_sel:WORD_1
	s_waitcnt vmcnt(3)
	v_cvt_pk_f32_fp8_e32 v[174:175], v176
	v_cvt_pk_f32_fp8_sdwa v[176:177], v176 src0_sel:WORD_1
	s_waitcnt vmcnt(2)
	v_cvt_pk_f32_fp8_e32 v[178:179], v180
	v_cvt_pk_f32_fp8_sdwa v[180:181], v180 src0_sel:WORD_1
	s_waitcnt vmcnt(1)
	v_cvt_pk_f32_fp8_e32 v[182:183], v184
	v_cvt_pk_f32_fp8_sdwa v[184:185], v184 src0_sel:WORD_1
	s_waitcnt vmcnt(0)
	v_cvt_pk_f32_fp8_e32 v[186:187], v188
	v_cvt_pk_f32_fp8_sdwa v[188:189], v188 src0_sel:WORD_1
	v_pk_fma_f32 v[106:107], v[66:67], v[108:109], v[106:107] op_sel_hi:[0,1,1]
	v_pk_fma_f32 v[96:97], v[66:67], v[110:111], v[96:97] op_sel_hi:[0,1,1]
	v_pk_fma_f32 v[104:105], v[66:67], v[130:131], v[104:105] op_sel_hi:[0,1,1]
	v_pk_fma_f32 v[94:95], v[66:67], v[132:133], v[94:95] op_sel_hi:[0,1,1]
	v_pk_fma_f32 v[102:103], v[66:67], v[134:135], v[102:103] op_sel_hi:[0,1,1]
	v_pk_fma_f32 v[92:93], v[66:67], v[136:137], v[92:93] op_sel_hi:[0,1,1]
	v_pk_fma_f32 v[100:101], v[66:67], v[138:139], v[100:101] op_sel_hi:[0,1,1]
	v_pk_fma_f32 v[90:91], v[66:67], v[140:141], v[90:91] op_sel_hi:[0,1,1]
	v_pk_fma_f32 v[98:99], v[66:67], v[142:143], v[98:99] op_sel_hi:[0,1,1]
	v_pk_fma_f32 v[88:89], v[66:67], v[144:145], v[88:89] op_sel_hi:[0,1,1]
	v_pk_fma_f32 v[86:87], v[66:67], v[146:147], v[86:87] op_sel_hi:[0,1,1]
	v_pk_fma_f32 v[84:85], v[66:67], v[148:149], v[84:85] op_sel_hi:[0,1,1]
	v_pk_fma_f32 v[82:83], v[66:67], v[150:151], v[82:83] op_sel_hi:[0,1,1]
	v_pk_fma_f32 v[80:81], v[66:67], v[152:153], v[80:81] op_sel_hi:[0,1,1]
	v_pk_fma_f32 v[78:79], v[66:67], v[154:155], v[78:79] op_sel_hi:[0,1,1]
	v_pk_fma_f32 v[76:77], v[66:67], v[156:157], v[76:77] op_sel_hi:[0,1,1]
	v_pk_fma_f32 v[96:97], v[74:75], v[160:161], v[96:97] op_sel_hi:[0,1,1]
	v_pk_fma_f32 v[106:107], v[74:75], v[158:159], v[106:107] op_sel_hi:[0,1,1]
	v_pk_fma_f32 v[94:95], v[74:75], v[164:165], v[94:95] op_sel_hi:[0,1,1]
	v_pk_fma_f32 v[104:105], v[74:75], v[162:163], v[104:105] op_sel_hi:[0,1,1]
	v_pk_fma_f32 v[92:93], v[74:75], v[168:169], v[92:93] op_sel_hi:[0,1,1]
	v_pk_fma_f32 v[102:103], v[74:75], v[166:167], v[102:103] op_sel_hi:[0,1,1]
	v_pk_fma_f32 v[90:91], v[74:75], v[172:173], v[90:91] op_sel_hi:[0,1,1]
	v_pk_fma_f32 v[100:101], v[74:75], v[170:171], v[100:101] op_sel_hi:[0,1,1]
	v_pk_fma_f32 v[88:89], v[74:75], v[176:177], v[88:89] op_sel_hi:[0,1,1]
	v_pk_fma_f32 v[98:99], v[74:75], v[174:175], v[98:99] op_sel_hi:[0,1,1]
	v_pk_fma_f32 v[84:85], v[74:75], v[180:181], v[84:85] op_sel_hi:[0,1,1]
	v_pk_fma_f32 v[86:87], v[74:75], v[178:179], v[86:87] op_sel_hi:[0,1,1]
	v_pk_fma_f32 v[80:81], v[74:75], v[184:185], v[80:81] op_sel_hi:[0,1,1]
	v_pk_fma_f32 v[82:83], v[74:75], v[182:183], v[82:83] op_sel_hi:[0,1,1]
	v_pk_fma_f32 v[76:77], v[74:75], v[188:189], v[76:77] op_sel_hi:[0,1,1]
	v_pk_fma_f32 v[78:79], v[74:75], v[186:187], v[78:79] op_sel_hi:[0,1,1]
	s_cbranch_scc0 .LBB0_2391
; #define GAS __attribute__((address_space(1)))
; #define LAS __attribute__((address_space(3)))
; __device__ __forceinline__ void phase_combine(const Frame& F, const Args& a, int layer) {
;     ...
;             const int r = modrow(row); bf16_t* xr = X + (size_t)row * D; float s = 0.f;
;             const LAS float* pg2 = P + (2 + 3 * r) * D;
; #pragma unroll
;             for (int i = 0; i < 8; ++i) { const int c = 4 * F.lane + 256 * i; const u32x2 p = *(const GAS u32x2*)(xr + c); const f32x4 xv = {bflo(p.x), bfhi(p.x), bflo(p.y), bfhi(p.y)};
;                 f[i] = xv * ALPHA + *(const LAS f32x4*)(pg2 + c) * f[i]; s += (f[i][0] + f[i][1]) + (f[i][2] + f[i][3]); }
	s_add_i32 s10, s12, 0xfffffe00
	s_ashr_i32 s13, s12, 31
	s_lshr_b32 s25, s10, 12
	s_lshl_b64 s[10:11], s[12:13], 11
	s_mulk_i32 s25, 0x6000
	s_cmpk_gt_i32 s12, 0x1ff
	s_cselect_b32 s25, s25, 0xc000
	s_lshl_b64 s[12:13], s[12:13], 12
	v_lshl_add_u64 v[74:75], v[70:71], 0, s[12:13]
	global_load_dwordx2 v[108:109], v[74:75], off
	global_load_dwordx2 v[110:111], v[74:75], off offset:512
	global_load_dwordx2 v[156:157], v[74:75], off offset:1024
	global_load_dwordx2 v[158:159], v[74:75], off offset:1536
	global_load_dwordx2 v[160:161], v[74:75], off offset:2048
	global_load_dwordx2 v[162:163], v[74:75], off offset:2560
	v_add_u32_e32 v130, s25, v113
	ds_read_b128 v[132:135], v130 offset:16384
	ds_read_b128 v[136:139], v130 offset:17408
	ds_read_b128 v[140:143], v130 offset:18432
	ds_read_b128 v[144:147], v130 offset:19456
	ds_read_b128 v[148:151], v130 offset:20480
	ds_read_b128 v[152:155], v130 offset:21504
	global_load_dwordx2 v[164:165], v[74:75], off offset:3072
	global_load_dwordx2 v[166:167], v[74:75], off offset:3584
	s_add_i32 s23, s23, 64
	s_waitcnt vmcnt(7)
	v_lshlrev_b32_e32 v168, 16, v108
	v_and_b32_e32 v169, 0xffff0000, v108
	v_lshlrev_b32_e32 v108, 16, v109
	v_and_b32_e32 v109, 0xffff0000, v109
	s_waitcnt vmcnt(6)
	v_lshlrev_b32_e32 v170, 16, v110
	v_and_b32_e32 v171, 0xffff0000, v110
	v_lshlrev_b32_e32 v110, 16, v111
	v_and_b32_e32 v111, 0xffff0000, v111
	s_waitcnt vmcnt(5)
	v_lshlrev_b32_e32 v172, 16, v156
	v_and_b32_e32 v173, 0xffff0000, v156
	v_lshlrev_b32_e32 v156, 16, v157
	v_and_b32_e32 v157, 0xffff0000, v157
	s_waitcnt vmcnt(4)
	v_lshlrev_b32_e32 v174, 16, v158
	v_and_b32_e32 v175, 0xffff0000, v158
	v_lshlrev_b32_e32 v158, 16, v159
	v_and_b32_e32 v159, 0xffff0000, v159
	s_waitcnt vmcnt(3)
	v_lshlrev_b32_e32 v176, 16, v160
	v_and_b32_e32 v177, 0xffff0000, v160
	v_pk_mul_f32 v[168:169], v[168:169], s[8:9] op_sel_hi:[1,0]
	v_pk_mul_f32 v[108:109], v[108:109], s[8:9] op_sel_hi:[1,0]
	v_pk_mul_f32 v[170:171], v[170:171], s[8:9] op_sel_hi:[1,0]
	v_pk_mul_f32 v[180:181], v[110:111], s[8:9] op_sel_hi:[1,0]
	v_pk_mul_f32 v[172:173], v[172:173], s[8:9] op_sel_hi:[1,0]
	v_pk_mul_f32 v[156:157], v[156:157], s[8:9] op_sel_hi:[1,0]
	v_pk_mul_f32 v[174:175], v[174:175], s[8:9] op_sel_hi:[1,0]
	v_pk_mul_f32 v[158:159], v[158:159], s[8:9] op_sel_hi:[1,0]
	v_pk_mul_f32 v[176:177], v[176:177], s[8:9] op_sel_hi:[1,0]
	s_waitcnt lgkmcnt(5)
	v_pk_fma_f32 v[108:109], v[96:97], v[134:135], v[108:109]
	v_pk_fma_f32 v[110:111], v[106:107], v[132:133], v[168:169]
	s_waitcnt lgkmcnt(4)
	v_pk_fma_f32 v[106:107], v[94:95], v[138:139], v[180:181]
	v_pk_fma_f32 v[104:105], v[104:105], v[136:137], v[170:171]
	s_waitcnt lgkmcnt(3)
	v_pk_fma_f32 v[96:97], v[92:93], v[142:143], v[156:157]
	v_pk_fma_f32 v[102:103], v[102:103], v[140:141], v[172:173]
	s_waitcnt lgkmcnt(2)
	v_pk_fma_f32 v[92:93], v[90:91], v[146:147], v[158:159]
	v_pk_fma_f32 v[94:95], v[100:101], v[144:145], v[174:175]
	s_waitcnt lgkmcnt(1)
	v_pk_fma_f32 v[90:91], v[98:99], v[148:149], v[176:177]
	v_mov_b32_e32 v98, v110
	v_mov_b32_e32 v99, v104
	v_mov_b32_e32 v100, v111
	v_mov_b32_e32 v101, v105
	v_mov_b32_e32 v132, v108
	v_mov_b32_e32 v133, v106
	v_mov_b32_e32 v134, v109
	v_mov_b32_e32 v135, v107
	v_lshlrev_b32_e32 v160, 16, v161
	v_and_b32_e32 v161, 0xffff0000, v161
	v_pk_mov_b32 v[136:137], v[102:103], v[96:97] op_sel:[1,0]
	v_mov_b32_e32 v138, v102
	v_mov_b32_e32 v139, v97
	v_pk_add_f32 v[98:99], v[98:99], v[100:101]
	v_pk_add_f32 v[100:101], v[132:133], v[134:135]
	v_pk_mul_f32 v[160:161], v[160:161], s[8:9] op_sel_hi:[1,0]
	v_pk_add_f32 v[132:133], v[136:137], v[138:139]
	v_pk_add_f32 v[98:99], v[98:99], v[100:101]
	v_pk_fma_f32 v[88:89], v[88:89], v[150:151], v[160:161]
	v_pk_add_f32 v[100:101], v[132:133], v[132:133] op_sel:[0,1] op_sel_hi:[1,0]
	v_add_f32_e32 v66, 0, v98
	v_add_f32_e32 v140, v94, v95
	v_add_f32_e32 v142, v92, v93
	v_mov_b32_e32 v145, v90
	v_mov_b32_e32 v141, v88
	v_mov_b32_e32 v143, v89
	v_mov_b32_e32 v101, v91
	v_add_f32_e32 v144, v66, v99
	v_pk_add_f32 v[134:135], v[140:141], v[142:143]
	v_pk_add_f32 v[98:99], v[144:145], v[100:101]
	s_waitcnt vmcnt(2)
	v_lshlrev_b32_e32 v178, 16, v162
	v_and_b32_e32 v179, 0xffff0000, v162
	v_lshlrev_b32_e32 v162, 16, v163
	v_and_b32_e32 v163, 0xffff0000, v163
	v_pk_add_f32 v[98:99], v[98:99], v[134:135]
	v_pk_mul_f32 v[100:101], v[162:163], s[8:9] op_sel_hi:[1,0]
	v_pk_add_f32 v[136:137], v[98:99], v[98:99] op_sel:[0,1] op_sel_hi:[1,0]
	v_pk_mul_f32 v[98:99], v[178:179], s[8:9] op_sel_hi:[1,0]
	s_waitcnt lgkmcnt(0)
	v_pk_fma_f32 v[84:85], v[84:85], v[154:155], v[100:101]
	v_pk_fma_f32 v[86:87], v[86:87], v[152:153], v[98:99]
	v_mov_b32_e32 v101, v85
	v_pk_mov_b32 v[98:99], v[86:87], v[84:85] op_sel:[1,0]
	v_mov_b32_e32 v100, v86
	v_pk_add_f32 v[98:99], v[98:99], v[100:101]
	s_waitcnt vmcnt(1)
	v_lshlrev_b32_e32 v132, 16, v164
	v_pk_add_f32 v[138:139], v[98:99], v[98:99] op_sel:[0,1] op_sel_hi:[1,0]
	ds_read_b128 v[98:101], v130 offset:22528
	v_and_b32_e32 v133, 0xffff0000, v164
	v_lshlrev_b32_e32 v134, 16, v165
	v_and_b32_e32 v135, 0xffff0000, v165
	v_pk_mul_f32 v[140:141], v[132:133], s[8:9] op_sel_hi:[1,0]
	v_pk_mul_f32 v[142:143], v[134:135], s[8:9] op_sel_hi:[1,0]
	ds_read_b128 v[132:135], v130 offset:23552
	s_waitcnt lgkmcnt(1)
	v_pk_fma_f32 v[80:81], v[80:81], v[100:101], v[142:143]
	v_pk_fma_f32 v[82:83], v[82:83], v[98:99], v[140:141]
	s_waitcnt vmcnt(0)
	v_lshlrev_b32_e32 v140, 16, v166
	v_and_b32_e32 v141, 0xffff0000, v166
	v_lshlrev_b32_e32 v142, 16, v167
	v_and_b32_e32 v143, 0xffff0000, v167
	v_pk_mul_f32 v[140:141], v[140:141], s[8:9] op_sel_hi:[1,0]
	v_pk_mul_f32 v[142:143], v[142:143], s[8:9] op_sel_hi:[1,0]
	s_waitcnt lgkmcnt(0)
; #define LAS __attribute__((address_space(3)))
; __device__ __forceinline__ void phase_combine(const Frame& F, const Args& a, int layer) {
;     ...
;                 f[i] = xv * ALPHA + *(const LAS f32x4*)(pg2 + c) * f[i]; s += (f[i][0] + f[i][1]) + (f[i][2] + f[i][3]); }
;             const float mean = wave_sum(s) * (1.0f / D); float ss = 0.f;
; #pragma unroll
;             for (int i = 0; i < 8; ++i) { f[i] = f[i] - mean; ss += (f[i][0] * f[i][0] + f[i][1] * f[i][1]) + (f[i][2] * f[i][2] + f[i][3] * f[i][3]); }
;             const float rstd = rsqrtf(wave_sum(ss) * (1.0f / D) + LN_EPS);
	v_pk_fma_f32 v[78:79], v[78:79], v[132:133], v[140:141]
	v_pk_fma_f32 v[76:77], v[76:77], v[134:135], v[142:143]
	v_add_f32_e32 v98, v82, v83
	v_add_f32_e32 v100, v80, v81
	v_mov_b32_e32 v137, v78
	v_mov_b32_e32 v139, v79
	v_mov_b32_e32 v99, v76
	v_mov_b32_e32 v101, v77
	v_pk_add_f32 v[132:133], v[136:137], v[138:139]
	v_pk_add_f32 v[98:99], v[98:99], v[100:101]
	s_nop 0
	v_pk_add_f32 v[98:99], v[132:133], v[98:99]
	s_nop 0
	v_add_f32_e32 v66, v98, v99
	s_waitcnt lgkmcnt(0)
	s_nop 1
	v_add_f32_dpp v66, v66, v66 quad_perm:[1,0,3,2] row_mask:0xf bank_mask:0xf
	s_waitcnt lgkmcnt(0)
	s_nop 1
	v_add_f32_dpp v66, v66, v66 quad_perm:[2,3,0,1] row_mask:0xf bank_mask:0xf
	s_waitcnt lgkmcnt(0)
	s_nop 1
	v_add_f32_dpp v66, v66, v66 row_half_mirror row_mask:0xf bank_mask:0xf
	s_waitcnt lgkmcnt(0)
	s_nop 1
	v_add_f32_dpp v66, v66, v66 row_mirror row_mask:0xf bank_mask:0xf
	v_mov_b32_e32 v98, v66
	s_nop 1
	v_permlane16_swap_b32 v98, v66
	s_waitcnt lgkmcnt(0)
	v_add_f32_e32 v66, v66, v98
	v_mov_b32_e32 v98, v66
	s_nop 1
	v_permlane32_swap_b32 v98, v66
	s_waitcnt lgkmcnt(0)
	v_add_f32_e32 v131, v66, v98
	v_fmamk_f32 v111, v131, 0xba000000, v111
	v_fmamk_f32 v105, v131, 0xba000000, v105
	v_fmamk_f32 v109, v131, 0xba000000, v109
	v_fmac_f32_e32 v110, 0xba000000, v131
	v_fmamk_f32 v107, v131, 0xba000000, v107
	v_fmac_f32_e32 v104, 0xba000000, v131
	v_mov_b32_e32 v100, v111
	v_mov_b32_e32 v101, v105
	v_fmac_f32_e32 v108, 0xba000000, v131
	v_fmac_f32_e32 v106, 0xba000000, v131
	v_mov_b32_e32 v98, v110
	v_mov_b32_e32 v99, v104
	v_pk_mul_f32 v[100:101], v[100:101], v[100:101]
	v_mov_b32_e32 v132, v109
	v_mov_b32_e32 v133, v107
	v_pk_fma_f32 v[98:99], v[98:99], v[98:99], v[100:101]
	v_mov_b32_e32 v100, v108
	v_mov_b32_e32 v101, v106
	v_pk_mul_f32 v[132:133], v[132:133], v[132:133]
	v_fmamk_f32 v103, v131, 0xba000000, v103
	v_pk_fma_f32 v[100:101], v[100:101], v[100:101], v[132:133]
	v_fmac_f32_e32 v102, 0xba000000, v131
	v_fmamk_f32 v97, v131, 0xba000000, v97
	v_fmac_f32_e32 v96, 0xba000000, v131
	v_pk_add_f32 v[98:99], v[98:99], v[100:101]
	v_pk_mul_f32 v[100:101], v[96:97], v[96:97]
	v_pk_mul_f32 v[132:133], v[102:103], v[102:103]
	v_fmac_f32_e32 v94, 0xba000000, v131
	v_pk_mov_b32 v[134:135], v[132:133], v[100:101] op_sel:[1,0]
	v_mov_b32_e32 v133, v101
	v_fmamk_f32 v95, v131, 0xba000000, v95
	v_fmac_f32_e32 v92, 0xba000000, v131
	v_mul_f32_e32 v66, v94, v94
	v_pk_add_f32 v[100:101], v[134:135], v[132:133]
	v_fmamk_f32 v93, v131, 0xba000000, v93
	v_pk_fma_f32 v[132:133], v[94:95], v[94:95], v[66:67] op_sel_hi:[1,1,0]
	v_mul_f32_e32 v66, v92, v92
	v_pk_add_f32 v[98:99], v[98:99], v[98:99] op_sel_hi:[0,1]
	v_pk_add_f32 v[100:101], v[100:101], v[100:101] op_sel_hi:[0,1]
	v_pk_fma_f32 v[134:135], v[92:93], v[92:93], v[66:67] op_sel_hi:[1,1,0]
	v_fmamk_f32 v89, v131, 0xba000000, v89
	v_fmac_f32_e32 v88, 0xba000000, v131
	v_fmamk_f32 v91, v131, 0xba000000, v91
	v_fmac_f32_e32 v90, 0xba000000, v131
	v_mul_f32_e32 v132, v90, v90
	v_mul_f32_e32 v134, v91, v91
	v_mul_f32_e32 v100, v88, v88
	v_mul_f32_e32 v98, v89, v89
	v_pk_add_f32 v[132:133], v[132:133], v[134:135]
	v_pk_add_f32 v[98:99], v[100:101], v[98:99]
	v_fmamk_f32 v87, v131, 0xba000000, v87
	v_fmac_f32_e32 v86, 0xba000000, v131
	v_fmamk_f32 v85, v131, 0xba000000, v85
	v_fmac_f32_e32 v84, 0xba000000, v131
	v_pk_add_f32 v[98:99], v[132:133], v[98:99]
	v_pk_mul_f32 v[100:101], v[84:85], v[84:85]
	v_pk_mul_f32 v[132:133], v[86:87], v[86:87]
	v_fmac_f32_e32 v82, 0xba000000, v131
	v_pk_mov_b32 v[134:135], v[132:133], v[100:101] op_sel:[1,0]
	v_mov_b32_e32 v133, v101
	v_fmamk_f32 v83, v131, 0xba000000, v83
	v_fmac_f32_e32 v80, 0xba000000, v131
	v_mul_f32_e32 v66, v82, v82
	v_pk_add_f32 v[100:101], v[134:135], v[132:133]
	v_fmamk_f32 v81, v131, 0xba000000, v81
	v_pk_fma_f32 v[132:133], v[82:83], v[82:83], v[66:67] op_sel_hi:[1,1,0]
	v_mul_f32_e32 v66, v80, v80
	v_pk_add_f32 v[98:99], v[98:99], v[98:99] op_sel_hi:[0,1]
	v_pk_add_f32 v[100:101], v[100:101], v[100:101] op_sel_hi:[0,1]
	v_pk_fma_f32 v[134:135], v[80:81], v[80:81], v[66:67] op_sel_hi:[1,1,0]
	v_fmamk_f32 v77, v131, 0xba000000, v77
	v_fmac_f32_e32 v76, 0xba000000, v131
	v_fmamk_f32 v79, v131, 0xba000000, v79
	v_fmac_f32_e32 v78, 0xba000000, v131
	v_mul_f32_e32 v132, v78, v78
	v_mul_f32_e32 v134, v79, v79
	v_mul_f32_e32 v100, v76, v76
	v_mul_f32_e32 v98, v77, v77
	v_pk_add_f32 v[132:133], v[132:133], v[134:135]
	v_pk_add_f32 v[98:99], v[100:101], v[98:99]
	s_nop 0
	v_pk_add_f32 v[98:99], v[132:133], v[98:99]
	s_nop 0
	v_add_f32_e32 v66, v98, v99
	s_waitcnt lgkmcnt(0)
	s_nop 1
	v_add_f32_dpp v66, v66, v66 quad_perm:[1,0,3,2] row_mask:0xf bank_mask:0xf
	s_waitcnt lgkmcnt(0)
	s_nop 1
	v_add_f32_dpp v66, v66, v66 quad_perm:[2,3,0,1] row_mask:0xf bank_mask:0xf
	s_waitcnt lgkmcnt(0)
	s_nop 1
	v_add_f32_dpp v66, v66, v66 row_half_mirror row_mask:0xf bank_mask:0xf
	s_waitcnt lgkmcnt(0)
	s_nop 1
	v_add_f32_dpp v66, v66, v66 row_mirror row_mask:0xf bank_mask:0xf
	v_mov_b32_e32 v98, v66
	s_nop 1
	v_permlane16_swap_b32 v98, v66
	s_waitcnt lgkmcnt(0)
	v_add_f32_e32 v66, v66, v98
	v_mov_b32_e32 v98, v66
	s_nop 1
	v_permlane32_swap_b32 v98, v66
	s_waitcnt lgkmcnt(0)
; #define GAS __attribute__((address_space(1)))
; #define LAS __attribute__((address_space(3)))
; __device__ __forceinline__ unsigned pk2(float lo, float hi) { return f2bf(lo) | (f2bf(hi) << 16); }
; __device__ __forceinline__ unsigned pk4_fp8(float a, float b, float c, float d) { int w = 0; w = __builtin_amdgcn_cvt_pk_fp8_f32(sat8(a), sat8(b), w, false); w = __builtin_amdgcn_cvt_pk_fp8_f32(sat8(c), sat8(d), w, true); return (unsigned)w; }
; __device__ __forceinline__ void phase_combine(const Frame& F, const Args& a, int layer) {
;     ...
;             const float rstd = rsqrtf(wave_sum(ss) * (1.0f / D) + LN_EPS);
;             if (layer == 0) { const LAS float* psc = P + (3 + 3 * r) * D; const LAS float* psh = P + (4 + 3 * r) * D;
; #pragma unroll
;                 for (int i = 0; i < 8; ++i) { const int c = 4 * F.lane + 256 * i;
;                     const f32x4 lat = f[i] * rstd * *(const LAS f32x4*)(P + c) + *(const LAS f32x4*)(P + D + c);
;                     { u32x2 wl; wl.x = pk2(lat[0], lat[1]); wl.y = pk2(lat[2], lat[3]); *(GAS u32x2*)(xr + c) = wl; }
;                     const f32x4 h = lat * *(const LAS f32x4*)(psc + c) + *(const LAS f32x4*)(psh + c);
;                     *(GAS unsigned*)((unsigned char*)A0 + (size_t)row * D + c) = pk4_fp8(h[0], h[1], h[2], h[3]); } }
	v_add_f32_e32 v66, v66, v98
	v_fmamk_f32 v66, v66, 0x3a000000, v122
	v_mul_f32_e32 v98, 0x4b800000, v66
	v_cmp_gt_f32_e32 vcc, s18, v66
	s_nop 1
	v_cndmask_b32_e32 v66, v66, v98, vcc
	v_rsq_f32_e32 v66, v66
	s_nop 0
	v_mul_f32_e32 v98, 0x45800000, v66
	v_cndmask_b32_e32 v66, v66, v98, vcc
	v_pk_mul_f32 v[98:99], v[110:111], v[66:67] op_sel_hi:[1,0]
	v_pk_mul_f32 v[100:101], v[108:109], v[66:67] op_sel_hi:[1,0]
	v_pk_fma_f32 v[142:143], v[2:3], v[98:99], v[10:11]
	v_pk_fma_f32 v[140:141], v[4:5], v[100:101], v[12:13]
	v_bfe_u32 v98, v142, 16, 1
	v_add3_u32 v98, v142, v98, s19
	v_bfe_u32 v99, v143, 16, 1
	v_lshrrev_b32_e32 v98, 16, v98
	v_add3_u32 v99, v143, v99, s19
	v_and_or_b32 v144, v99, s17, v98
	v_bfe_u32 v98, v140, 16, 1
	v_add3_u32 v98, v140, v98, s19
	v_lshrrev_b32_e32 v131, 16, v98
	ds_read_b128 v[98:101], v130 offset:24576
	ds_read_b128 v[108:111], v130 offset:32768
	v_bfe_u32 v132, v141, 16, 1
	v_add3_u32 v145, v141, v132, s19
	ds_read_b128 v[132:135], v130 offset:25600
	ds_read_b128 v[136:139], v130 offset:33792
	v_and_or_b32 v145, v145, s17, v131
	s_waitcnt lgkmcnt(2)
	v_pk_fma_f32 v[98:99], v[98:99], v[142:143], v[108:109]
	v_mov_b32_e32 v108, 0
	v_med3_f32 v98, v98, s20, v123
	v_med3_f32 v99, v99, s20, v123
	v_cvt_pk_fp8_f32 v108, v98, v99
	v_pk_fma_f32 v[98:99], v[100:101], v[140:141], v[110:111]
	v_pk_mul_f32 v[100:101], v[104:105], v[66:67] op_sel_hi:[1,0]
	v_pk_mul_f32 v[104:105], v[106:107], v[66:67] op_sel_hi:[1,0]
	v_pk_fma_f32 v[100:101], v[6:7], v[100:101], v[14:15]
	v_med3_f32 v98, v98, s20, v123
	v_bfe_u32 v106, v100, 16, 1
	v_bfe_u32 v107, v101, 16, 1
	v_med3_f32 v99, v99, s20, v123
	v_add3_u32 v106, v100, v106, s19
	v_add3_u32 v107, v101, v107, s19
	s_waitcnt lgkmcnt(0)
	v_pk_fma_f32 v[100:101], v[132:133], v[100:101], v[136:137]
	v_cvt_pk_fp8_f32 v108, v98, v99 op_sel:[0,0,1]
	v_med3_f32 v100, v100, s20, v123
	v_med3_f32 v101, v101, s20, v123
	v_mov_b32_e32 v109, 0
	v_cvt_pk_fp8_f32 v109, v100, v101
	v_pk_fma_f32 v[104:105], v[8:9], v[104:105], v[16:17]
	v_lshrrev_b32_e32 v106, 16, v106
	v_lshl_add_u64 v[98:99], v[72:73], 0, s[10:11]
	v_and_or_b32 v106, v107, s17, v106
	v_bfe_u32 v107, v104, 16, 1
	v_pk_fma_f32 v[100:101], v[134:135], v[104:105], v[138:139]
	global_store_dwordx2 v[74:75], v[144:145], off
	global_store_dword v[98:99], v108, off
	v_add3_u32 v107, v104, v107, s19
	v_bfe_u32 v108, v105, 16, 1
	v_med3_f32 v100, v100, s20, v123
	v_med3_f32 v101, v101, s20, v123
	v_lshrrev_b32_e32 v107, 16, v107
	v_cvt_pk_fp8_f32 v109, v100, v101 op_sel:[0,0,1]
	v_add3_u32 v100, v105, v108, s19
	v_and_or_b32 v107, v100, s17, v107
	v_pk_mul_f32 v[100:101], v[102:103], v[66:67] op_sel_hi:[1,0]
	v_pk_mul_f32 v[96:97], v[96:97], v[66:67] op_sel_hi:[1,0]
	v_pk_fma_f32 v[136:137], v[18:19], v[100:101], v[26:27]
	v_pk_fma_f32 v[96:97], v[20:21], v[96:97], v[28:29]
	v_bfe_u32 v100, v136, 16, 1
	v_add3_u32 v100, v136, v100, s19
	v_bfe_u32 v101, v137, 16, 1
	v_lshrrev_b32_e32 v100, 16, v100
	v_add3_u32 v101, v137, v101, s19
	global_store_dwordx2 v[74:75], v[106:107], off offset:512
	global_store_dword v[98:99], v109, off offset:256
	v_and_or_b32 v138, v101, s17, v100
	v_bfe_u32 v100, v96, 16, 1
	v_add3_u32 v108, v96, v100, s19
	ds_read_b128 v[100:103], v130 offset:26624
	ds_read_b128 v[104:107], v130 offset:34816
	v_lshrrev_b32_e32 v131, 16, v108
	ds_read_b128 v[108:111], v130 offset:27648
	ds_read_b128 v[132:135], v130 offset:35840
	v_bfe_u32 v139, v97, 16, 1
	v_pk_mul_f32 v[94:95], v[94:95], v[66:67] op_sel_hi:[1,0]
	s_waitcnt lgkmcnt(2)
	v_pk_fma_f32 v[100:101], v[100:101], v[136:137], v[104:105]
	v_mov_b32_e32 v104, 0
	v_med3_f32 v100, v100, s20, v123
	v_med3_f32 v101, v101, s20, v123
	v_cvt_pk_fp8_f32 v104, v100, v101
	v_pk_fma_f32 v[100:101], v[102:103], v[96:97], v[106:107]
	v_pk_fma_f32 v[94:95], v[22:23], v[94:95], v[30:31]
	v_med3_f32 v96, v100, s20, v123
	v_med3_f32 v100, v101, s20, v123
	v_cvt_pk_fp8_f32 v104, v96, v100 op_sel:[0,0,1]
	v_add3_u32 v96, v97, v139, s19
	v_and_or_b32 v139, v96, s17, v131
	v_bfe_u32 v96, v94, 16, 1
	v_bfe_u32 v97, v95, 16, 1
	v_add3_u32 v96, v94, v96, s19
	v_add3_u32 v97, v95, v97, s19
	s_waitcnt lgkmcnt(0)
; #define GAS __attribute__((address_space(1)))
; #define LAS __attribute__((address_space(3)))
; __device__ __forceinline__ unsigned pk2(float lo, float hi) { return f2bf(lo) | (f2bf(hi) << 16); }
; __device__ __forceinline__ unsigned pk4_fp8(float a, float b, float c, float d) { int w = 0; w = __builtin_amdgcn_cvt_pk_fp8_f32(sat8(a), sat8(b), w, false); w = __builtin_amdgcn_cvt_pk_fp8_f32(sat8(c), sat8(d), w, true); return (unsigned)w; }
; __device__ __forceinline__ void phase_combine(const Frame& F, const Args& a, int layer) {
;     ...
;             if (layer == 0) { const LAS float* psc = P + (3 + 3 * r) * D; const LAS float* psh = P + (4 + 3 * r) * D;
; #pragma unroll
;                 for (int i = 0; i < 8; ++i) { const int c = 4 * F.lane + 256 * i;
;                     const f32x4 lat = f[i] * rstd * *(const LAS f32x4*)(P + c) + *(const LAS f32x4*)(P + D + c);
;                     { u32x2 wl; wl.x = pk2(lat[0], lat[1]); wl.y = pk2(lat[2], lat[3]); *(GAS u32x2*)(xr + c) = wl; }
;                     const f32x4 h = lat * *(const LAS f32x4*)(psc + c) + *(const LAS f32x4*)(psh + c);
;                     *(GAS unsigned*)((unsigned char*)A0 + (size_t)row * D + c) = pk4_fp8(h[0], h[1], h[2], h[3]); } }
	v_pk_fma_f32 v[94:95], v[108:109], v[94:95], v[132:133]
	v_mov_b32_e32 v101, 0
	v_med3_f32 v94, v94, s20, v123
	v_med3_f32 v95, v95, s20, v123
	v_pk_mul_f32 v[92:93], v[92:93], v[66:67] op_sel_hi:[1,0]
	v_cvt_pk_fp8_f32 v101, v94, v95
	v_pk_fma_f32 v[92:93], v[24:25], v[92:93], v[32:33]
	v_lshrrev_b32_e32 v96, 16, v96
	v_and_or_b32 v96, v97, s17, v96
	v_bfe_u32 v97, v92, 16, 1
	v_pk_fma_f32 v[94:95], v[110:111], v[92:93], v[134:135]
	v_add3_u32 v97, v92, v97, s19
	v_med3_f32 v92, v94, s20, v123
	v_med3_f32 v94, v95, s20, v123
	v_bfe_u32 v100, v93, 16, 1
	v_cvt_pk_fp8_f32 v101, v92, v94 op_sel:[0,0,1]
	v_lshrrev_b32_e32 v97, 16, v97
	v_add3_u32 v92, v93, v100, s19
	v_pk_mul_f32 v[90:91], v[90:91], v[66:67] op_sel_hi:[1,0]
	v_and_or_b32 v97, v92, s17, v97
	v_pk_mul_f32 v[88:89], v[88:89], v[66:67] op_sel_hi:[1,0]
	v_pk_fma_f32 v[108:109], v[34:35], v[90:91], v[42:43]
	global_store_dwordx2 v[74:75], v[138:139], off offset:1024
	global_store_dword v[98:99], v104, off offset:512
	global_store_dwordx2 v[74:75], v[96:97], off offset:1536
	global_store_dword v[98:99], v101, off offset:768
	v_pk_fma_f32 v[96:97], v[36:37], v[88:89], v[44:45]
	v_bfe_u32 v88, v108, 16, 1
	v_add3_u32 v88, v108, v88, s19
	v_bfe_u32 v89, v109, 16, 1
	v_lshrrev_b32_e32 v88, 16, v88
	v_add3_u32 v89, v109, v89, s19
	v_and_or_b32 v110, v89, s17, v88
	v_bfe_u32 v88, v96, 16, 1
	v_add3_u32 v100, v96, v88, s19
	ds_read_b128 v[88:91], v130 offset:28672
	ds_read_b128 v[92:95], v130 offset:36864
	v_lshrrev_b32_e32 v111, 16, v100
	ds_read_b128 v[100:103], v130 offset:29696
	ds_read_b128 v[104:107], v130 offset:37888
	v_bfe_u32 v131, v97, 16, 1
	v_pk_mul_f32 v[86:87], v[86:87], v[66:67] op_sel_hi:[1,0]
	s_waitcnt lgkmcnt(2)
	v_pk_fma_f32 v[88:89], v[88:89], v[108:109], v[92:93]
	v_mov_b32_e32 v92, 0
	v_med3_f32 v88, v88, s20, v123
	v_med3_f32 v89, v89, s20, v123
	v_cvt_pk_fp8_f32 v92, v88, v89
	v_pk_fma_f32 v[88:89], v[90:91], v[96:97], v[94:95]
	v_pk_fma_f32 v[86:87], v[86:87], v[38:39], v[46:47]
	v_med3_f32 v88, v88, s20, v123
	v_med3_f32 v89, v89, s20, v123
	v_cvt_pk_fp8_f32 v92, v88, v89 op_sel:[0,0,1]
	v_add3_u32 v88, v97, v131, s19
	v_and_or_b32 v111, v88, s17, v111
	v_bfe_u32 v88, v86, 16, 1
	v_bfe_u32 v89, v87, 16, 1
	v_add3_u32 v88, v86, v88, s19
	v_add3_u32 v89, v87, v89, s19
	s_waitcnt lgkmcnt(0)
	v_pk_fma_f32 v[86:87], v[86:87], v[100:101], v[104:105]
	v_mov_b32_e32 v91, 0
	v_med3_f32 v86, v86, s20, v123
	v_med3_f32 v87, v87, s20, v123
	v_pk_mul_f32 v[84:85], v[84:85], v[66:67] op_sel_hi:[1,0]
	v_cvt_pk_fp8_f32 v91, v86, v87
	v_pk_fma_f32 v[84:85], v[84:85], v[40:41], v[48:49]
	v_lshrrev_b32_e32 v88, 16, v88
	v_and_or_b32 v88, v89, s17, v88
	v_bfe_u32 v89, v84, 16, 1
	v_pk_fma_f32 v[86:87], v[84:85], v[102:103], v[106:107]
	v_pk_mul_f32 v[82:83], v[82:83], v[66:67] op_sel_hi:[1,0]
	v_add3_u32 v89, v84, v89, s19
	v_med3_f32 v84, v86, s20, v123
	v_med3_f32 v86, v87, s20, v123
	v_pk_mul_f32 v[80:81], v[80:81], v[66:67] op_sel_hi:[1,0]
	v_pk_fma_f32 v[100:101], v[82:83], v[50:51], v[58:59]
	v_bfe_u32 v90, v85, 16, 1
	v_cvt_pk_fp8_f32 v91, v84, v86 op_sel:[0,0,1]
	v_pk_fma_f32 v[96:97], v[80:81], v[52:53], v[60:61]
	v_bfe_u32 v80, v100, 16, 1
	v_lshrrev_b32_e32 v89, 16, v89
	v_add3_u32 v84, v85, v90, s19
	v_add3_u32 v80, v100, v80, s19
	v_bfe_u32 v81, v101, 16, 1
	v_and_or_b32 v89, v84, s17, v89
	v_lshrrev_b32_e32 v80, 16, v80
	v_add3_u32 v81, v101, v81, s19
	global_store_dwordx2 v[74:75], v[110:111], off offset:2048
	global_store_dword v[98:99], v92, off offset:1024
	global_store_dwordx2 v[74:75], v[88:89], off offset:2560
	global_store_dword v[98:99], v91, off offset:1280
	v_and_or_b32 v102, v81, s17, v80
	v_bfe_u32 v80, v96, 16, 1
	v_add3_u32 v88, v96, v80, s19
	ds_read_b128 v[80:83], v130 offset:30720
	ds_read_b128 v[84:87], v130 offset:38912
	v_lshrrev_b32_e32 v103, 16, v88
	ds_read_b128 v[88:91], v130 offset:31744
	ds_read_b128 v[92:95], v130 offset:39936
	v_bfe_u32 v104, v97, 16, 1
	v_pk_mul_f32 v[78:79], v[78:79], v[66:67] op_sel_hi:[1,0]
	s_waitcnt lgkmcnt(2)
	v_pk_fma_f32 v[80:81], v[100:101], v[80:81], v[84:85]
	v_mov_b32_e32 v84, 0
	v_med3_f32 v80, v80, s20, v123
	v_med3_f32 v81, v81, s20, v123
	v_cvt_pk_fp8_f32 v84, v80, v81
	v_pk_fma_f32 v[80:81], v[96:97], v[82:83], v[86:87]
	v_pk_fma_f32 v[78:79], v[78:79], v[54:55], v[62:63]
	v_med3_f32 v80, v80, s20, v123
	v_med3_f32 v81, v81, s20, v123
	v_cvt_pk_fp8_f32 v84, v80, v81 op_sel:[0,0,1]
	v_add3_u32 v80, v97, v104, s19
	v_and_or_b32 v103, v80, s17, v103
	v_pk_mul_f32 v[76:77], v[76:77], v[66:67] op_sel_hi:[1,0]
	v_bfe_u32 v66, v78, 16, 1
	v_bfe_u32 v80, v79, 16, 1
	v_add3_u32 v66, v78, v66, s19
	v_add3_u32 v80, v79, v80, s19
	s_waitcnt lgkmcnt(0)
	v_pk_fma_f32 v[78:79], v[78:79], v[88:89], v[92:93]
	v_mov_b32_e32 v82, 0
	v_med3_f32 v78, v78, s20, v123
	v_med3_f32 v79, v79, s20, v123
	v_cvt_pk_fp8_f32 v82, v78, v79
	v_pk_fma_f32 v[76:77], v[76:77], v[56:57], v[64:65]
	v_lshrrev_b32_e32 v66, 16, v66
	v_and_or_b32 v80, v80, s17, v66
	v_bfe_u32 v66, v76, 16, 1
	v_pk_fma_f32 v[78:79], v[76:77], v[90:91], v[94:95]
	v_add3_u32 v66, v76, v66, s19
	v_med3_f32 v76, v78, s20, v123
	v_med3_f32 v78, v79, s20, v123
	v_bfe_u32 v81, v77, 16, 1
	v_cvt_pk_fp8_f32 v82, v76, v78 op_sel:[0,0,1]
	v_lshrrev_b32_e32 v66, 16, v66
	v_add3_u32 v76, v77, v81, s19
	s_add_i32 s10, s24, 8
	v_and_or_b32 v81, v76, s17, v66
	s_cmp_gt_u32 s24, 25
	s_mov_b32 s24, s10
	global_store_dwordx2 v[74:75], v[102:103], off offset:3072
	global_store_dword v[98:99], v84, off offset:1536
	global_store_dwordx2 v[74:75], v[80:81], off offset:3584
	global_store_dword v[98:99], v82, off offset:1792
	s_cbranch_scc0 .LBB0_2390
	s_branch .LBB0_2387

; #define GAS __attribute__((address_space(1)))
; __device__ __forceinline__ const float* modp(const unsigned char* ws, int layer, int r, int chunk) { return (const float*)(ws + WS_MOD) + ((size_t)(layer * 3 + r) * 6 + chunk) * D; }
; __device__ __forceinline__ void phase_ln_router(const Frame& F, const Args& a, int layer) {
;     ...
;         for (int j = F.wave; j < TPB; j += 8) { const int row = rb + j; bf16_t* xr = X + (size_t)row * D;
;             f32x4 v[8]; float s = 0.f;
; #pragma unroll
;             for (int i = 0; i < 8; ++i) { const u32x2 p = *(const GAS u32x2*)(xr + 4 * F.lane + 256 * i); v[i] = (f32x4){bflo(p.x), bfhi(p.x), bflo(p.y), bfhi(p.y)}; s += (v[i][0] + v[i][1]) + (v[i][2] + v[i][3]); }
;             const int r = modrow(row);
;             if (r != rcur) { rcur = r; const float* sh2 = modp(F.ws, layer, r, 3); const float* sc2 = modp(F.ws, layer, r, 4);
; #pragma unroll
;                 for (int i = 0; i < 8; ++i) { const int c = 4 * F.lane + 256 * i; psc[i] = *(const GAS f32x4*)(sc2 + c) + 1.0f; psh[i] = *(const GAS f32x4*)(sh2 + c); } }
;             const float mean = wave_sum(s) * (1.0f / D); float ss = 0.f;
; #pragma unroll
;             for (int i = 0; i < 8; ++i) { v[i] = v[i] - mean; ss += (v[i][0] * v[i][0] + v[i][1] * v[i][1]) + (v[i][2] * v[i][2] + v[i][3] * v[i][3]); }
;             const float rstd = rsqrtf(wave_sum(ss) * (1.0f / D) + LN_EPS);
.LBB0_3036:
	s_waitcnt vmcnt(0)
	v_lshlrev_b32_e32 v92, 16, v86
	v_and_b32_e32 v93, 0xffff0000, v86
	v_lshlrev_b32_e32 v98, 16, v87
	v_and_b32_e32 v99, 0xffff0000, v87
	v_add_f32_e32 v86, v92, v93
	v_add_f32_e32 v87, v98, v99
	v_lshlrev_b32_e32 v100, 16, v84
	v_and_b32_e32 v101, 0xffff0000, v84
	v_lshlrev_b32_e32 v102, 16, v85
	v_and_b32_e32 v103, 0xffff0000, v85
	v_add_f32_e32 v86, v86, v87
	v_add_f32_e32 v84, v100, v101
	v_add_f32_e32 v85, v102, v103
	v_lshlrev_b32_e32 v104, 16, v82
	v_and_b32_e32 v105, 0xffff0000, v82
	v_lshlrev_b32_e32 v106, 16, v83
	v_and_b32_e32 v107, 0xffff0000, v83
	v_add_f32_e32 v86, 0, v86
	v_add_f32_e32 v84, v84, v85
	v_add_f32_e32 v82, v104, v105
	v_add_f32_e32 v83, v106, v107
	v_lshlrev_b32_e32 v94, 16, v80
	v_and_b32_e32 v95, 0xffff0000, v80
	v_lshlrev_b32_e32 v96, 16, v81
	v_and_b32_e32 v97, 0xffff0000, v81
	v_add_f32_e32 v84, v86, v84
	v_add_f32_e32 v82, v82, v83
	v_add_f32_e32 v80, v94, v95
	v_add_f32_e32 v81, v96, v97
	v_lshlrev_b32_e32 v86, 16, v76
	v_and_b32_e32 v87, 0xffff0000, v76
	v_lshlrev_b32_e32 v88, 16, v77
	v_and_b32_e32 v89, 0xffff0000, v77
	v_add_f32_e32 v82, v84, v82
	v_add_f32_e32 v80, v80, v81
	v_add_f32_e32 v76, v86, v87
	v_add_f32_e32 v77, v88, v89
	v_add_f32_e32 v80, v82, v80
	v_add_f32_e32 v76, v76, v77
	v_add_f32_e32 v76, v80, v76
	v_lshlrev_b32_e32 v80, 16, v72
	v_and_b32_e32 v81, 0xffff0000, v72
	v_lshlrev_b32_e32 v82, 16, v73
	v_and_b32_e32 v83, 0xffff0000, v73
	v_add_f32_e32 v72, v80, v81
	v_add_f32_e32 v73, v82, v83
	v_add_f32_e32 v72, v72, v73
	v_add_f32_e32 v76, v76, v72
	v_lshlrev_b32_e32 v72, 16, v74
	v_and_b32_e32 v73, 0xffff0000, v74
	v_lshlrev_b32_e32 v74, 16, v75
	v_and_b32_e32 v75, 0xffff0000, v75
	v_add_f32_e32 v77, v72, v73
	v_add_f32_e32 v84, v74, v75
	v_add_f32_e32 v77, v77, v84
	v_add_f32_e32 v84, v76, v77
	v_lshlrev_b32_e32 v76, 16, v78
	v_and_b32_e32 v77, 0xffff0000, v78
	v_lshlrev_b32_e32 v78, 16, v79
	v_and_b32_e32 v79, 0xffff0000, v79
	v_add_f32_e32 v85, v76, v77
	v_add_f32_e32 v90, v78, v79
	v_add_f32_e32 v85, v85, v90
	v_add_f32_e32 v84, v84, v85
	s_mov_b32 s0, 0x800000
	v_mov_b32_e32 v188, 0
	s_add_i32 s22, s30, 8
	s_cmp_gt_u32 s30, 23
	s_waitcnt lgkmcnt(0)
	s_nop 1
	v_add_f32_dpp v84, v84, v84 quad_perm:[1,0,3,2] row_mask:0xf bank_mask:0xf
	s_waitcnt lgkmcnt(0)
	s_nop 1
	v_add_f32_dpp v84, v84, v84 quad_perm:[2,3,0,1] row_mask:0xf bank_mask:0xf
	s_waitcnt lgkmcnt(0)
	s_nop 1
	v_add_f32_dpp v84, v84, v84 row_half_mirror row_mask:0xf bank_mask:0xf
	s_waitcnt lgkmcnt(0)
	s_nop 1
	v_add_f32_dpp v84, v84, v84 row_mirror row_mask:0xf bank_mask:0xf
	v_mov_b32_e32 v85, v84
	s_nop 1
	v_permlane16_swap_b32 v85, v84
	s_waitcnt lgkmcnt(0)
	v_add_f32_e32 v84, v84, v85
	v_mov_b32_e32 v85, v84
	s_nop 1
	v_permlane32_swap_b32 v85, v84
	s_waitcnt lgkmcnt(0)
	v_add_f32_e32 v90, v84, v85
	v_fmac_f32_e32 v93, 0xba000000, v90
	v_fmac_f32_e32 v101, 0xba000000, v90
	v_fmac_f32_e32 v99, 0xba000000, v90
	v_fmac_f32_e32 v92, 0xba000000, v90
	v_fmac_f32_e32 v103, 0xba000000, v90
	v_fmac_f32_e32 v100, 0xba000000, v90
	v_mov_b32_e32 v152, v93
	v_mov_b32_e32 v153, v101
	v_fmac_f32_e32 v98, 0xba000000, v90
	v_fmac_f32_e32 v102, 0xba000000, v90
	v_mov_b32_e32 v84, v92
	v_mov_b32_e32 v85, v100
	v_pk_mul_f32 v[152:153], v[152:153], v[152:153]
	v_mov_b32_e32 v176, v99
	v_mov_b32_e32 v177, v103
	v_pk_fma_f32 v[84:85], v[84:85], v[84:85], v[152:153]
	v_mov_b32_e32 v152, v98
	v_mov_b32_e32 v153, v102
	v_pk_mul_f32 v[176:177], v[176:177], v[176:177]
	v_fmac_f32_e32 v105, 0xba000000, v90
	v_pk_fma_f32 v[152:153], v[152:153], v[152:153], v[176:177]
	v_fmac_f32_e32 v104, 0xba000000, v90
	v_pk_add_f32 v[84:85], v[84:85], v[152:153]
	v_fmac_f32_e32 v107, 0xba000000, v90
	v_fmac_f32_e32 v106, 0xba000000, v90
	v_pk_add_f32 v[84:85], v[84:85], v[84:85] op_sel_hi:[0,1]
	v_pk_mul_f32 v[152:153], v[106:107], v[106:107]
	v_pk_mul_f32 v[176:177], v[104:105], v[104:105]
	v_fmac_f32_e32 v94, 0xba000000, v90
	v_pk_mov_b32 v[178:179], v[176:177], v[152:153] op_sel:[1,0]
	v_mov_b32_e32 v177, v153
	v_fmac_f32_e32 v95, 0xba000000, v90
	v_fmac_f32_e32 v96, 0xba000000, v90
	v_mul_f32_e32 v84, v94, v94
	v_pk_add_f32 v[152:153], v[178:179], v[176:177]
	v_fmac_f32_e32 v97, 0xba000000, v90
	v_pk_fma_f32 v[176:177], v[94:95], v[94:95], v[84:85] op_sel_hi:[1,1,0]
	v_mul_f32_e32 v84, v96, v96
	v_pk_add_f32 v[152:153], v[152:153], v[152:153] op_sel_hi:[0,1]
	v_pk_fma_f32 v[178:179], v[96:97], v[96:97], v[84:85] op_sel_hi:[1,1,0]
	v_fmac_f32_e32 v89, 0xba000000, v90
	v_fmac_f32_e32 v88, 0xba000000, v90
	v_fmac_f32_e32 v87, 0xba000000, v90
	v_fmac_f32_e32 v86, 0xba000000, v90
	v_mul_f32_e32 v176, v86, v86
	v_mul_f32_e32 v178, v87, v87
	v_mul_f32_e32 v152, v88, v88
	v_mul_f32_e32 v84, v89, v89
	v_pk_add_f32 v[176:177], v[176:177], v[178:179]
	v_pk_add_f32 v[84:85], v[152:153], v[84:85]
	v_fmac_f32_e32 v81, 0xba000000, v90
	v_pk_add_f32 v[84:85], v[176:177], v[84:85]
	v_fmac_f32_e32 v80, 0xba000000, v90
	v_fmac_f32_e32 v83, 0xba000000, v90
	v_fmac_f32_e32 v82, 0xba000000, v90
	v_pk_add_f32 v[84:85], v[84:85], v[84:85] op_sel_hi:[0,1]
	v_pk_mul_f32 v[152:153], v[82:83], v[82:83]
	v_pk_mul_f32 v[184:185], v[80:81], v[80:81]
	v_fmac_f32_e32 v72, 0xba000000, v90
	v_pk_mov_b32 v[186:187], v[184:185], v[152:153] op_sel:[1,0]
	v_mov_b32_e32 v185, v153
	v_fmac_f32_e32 v73, 0xba000000, v90
	v_fmac_f32_e32 v74, 0xba000000, v90
	v_mul_f32_e32 v84, v72, v72
	v_pk_add_f32 v[152:153], v[186:187], v[184:185]
	v_fmac_f32_e32 v75, 0xba000000, v90
	v_pk_fma_f32 v[184:185], v[72:73], v[72:73], v[84:85] op_sel_hi:[1,1,0]
	v_mul_f32_e32 v84, v74, v74
	v_pk_add_f32 v[152:153], v[152:153], v[152:153] op_sel_hi:[0,1]
	v_pk_fma_f32 v[186:187], v[74:75], v[74:75], v[84:85] op_sel_hi:[1,1,0]
	v_fmac_f32_e32 v79, 0xba000000, v90
	v_fmac_f32_e32 v78, 0xba000000, v90
	v_fmac_f32_e32 v77, 0xba000000, v90
	v_fmac_f32_e32 v76, 0xba000000, v90
	v_mul_f32_e32 v184, v76, v76
	v_mul_f32_e32 v186, v77, v77
	v_mul_f32_e32 v152, v78, v78
	v_mul_f32_e32 v84, v79, v79
	v_pk_add_f32 v[184:185], v[184:185], v[186:187]
	v_pk_add_f32 v[84:85], v[152:153], v[84:85]
	s_nop 0
	v_pk_add_f32 v[84:85], v[184:185], v[84:85]
	s_nop 0
	v_add_f32_e32 v84, v84, v85
	s_waitcnt lgkmcnt(0)
; #define GAS __attribute__((address_space(1)))
; #define LAS __attribute__((address_space(3)))
; __device__ __forceinline__ unsigned pk2(float lo, float hi) { return f2bf(lo) | (f2bf(hi) << 16); }
; __device__ __forceinline__ unsigned pk4_fp8(float a, float b, float c, float d) { int w = 0; w = __builtin_amdgcn_cvt_pk_fp8_f32(sat8(a), sat8(b), w, false); w = __builtin_amdgcn_cvt_pk_fp8_f32(sat8(c), sat8(d), w, true); return (unsigned)w; }
; __device__ __forceinline__ void phase_ln_router(const Frame& F, const Args& a, int layer) {
;     ...
;             const float rstd = rsqrtf(wave_sum(ss) * (1.0f / D) + LN_EPS);
; #pragma unroll
;             for (int i = 0; i < 8; ++i) { const int c = 4 * F.lane + 256 * i;
;                 const f32x4 lat = v[i] * rstd * *(const GAS f32x4*)(lng + c) + *(const GAS f32x4*)(lnb + c);
;                 { u32x2 wl; wl.x = pk2(lat[0], lat[1]); wl.y = pk2(lat[2], lat[3]); *(GAS u32x2*)(xr + c) = wl; }
;                 const f32x4 h = lat * psc[i] + psh[i];
;                 u32x2 w; w.x = pk2(h[0], h[1]); w.y = pk2(h[2], h[3]); *(GAS unsigned*)((unsigned char*)A0 + (size_t)row * D + c) = pk4_fp8(h[0], h[1], h[2], h[3]);
;                 *(LAS u32x2*)(hb + j * HB_LD + c) = w; } }
	s_nop 1
	v_add_f32_dpp v84, v84, v84 quad_perm:[1,0,3,2] row_mask:0xf bank_mask:0xf
	s_waitcnt lgkmcnt(0)
	s_nop 1
	v_add_f32_dpp v84, v84, v84 quad_perm:[2,3,0,1] row_mask:0xf bank_mask:0xf
	s_waitcnt lgkmcnt(0)
	s_nop 1
	v_add_f32_dpp v84, v84, v84 row_half_mirror row_mask:0xf bank_mask:0xf
	s_waitcnt lgkmcnt(0)
	s_nop 1
	v_add_f32_dpp v84, v84, v84 row_mirror row_mask:0xf bank_mask:0xf
	v_mov_b32_e32 v85, v84
	s_nop 1
	v_permlane16_swap_b32 v85, v84
	s_waitcnt lgkmcnt(0)
	v_add_f32_e32 v84, v84, v85
	v_mov_b32_e32 v85, v84
	s_nop 1
	v_permlane32_swap_b32 v85, v84
	s_waitcnt lgkmcnt(0)
	v_add_f32_e32 v84, v84, v85
	v_fmamk_f32 v84, v84, 0x3a000000, v167
	v_mul_f32_e32 v85, 0x4b800000, v84
	v_cmp_gt_f32_e32 vcc, s0, v84
	s_mov_b64 s[0:1], 0x34000000
	s_nop 0
	v_cndmask_b32_e32 v84, v84, v85, vcc
	v_rsq_f32_e32 v90, v84
	v_lshl_add_u64 v[84:85], v[70:71], 0, s[0:1]
	s_mov_b64 s[0:1], 0x34000200
	v_mul_f32_e32 v152, 0x45800000, v90
	v_cndmask_b32_e32 v90, v90, v152, vcc
	v_pk_mul_f32 v[92:93], v[92:93], v[90:91] op_sel_hi:[1,0]
	v_pk_mul_f32 v[98:99], v[98:99], v[90:91] op_sel_hi:[1,0]
	v_pk_fma_f32 v[92:93], v[208:209], v[92:93], v[242:243]
	v_pk_fma_f32 v[98:99], v[210:211], v[98:99], v[244:245]
	v_bfe_u32 v152, v92, 16, 1
	v_add3_u32 v152, v92, v152, s39
	v_bfe_u32 v153, v93, 16, 1
	v_lshrrev_b32_e32 v152, 16, v152
	v_add3_u32 v153, v93, v153, s39
	v_and_or_b32 v152, v153, s38, v152
	v_bfe_u32 v153, v98, 16, 1
	v_add3_u32 v153, v98, v153, s39
	v_bfe_u32 v175, v99, 16, 1
	v_lshrrev_b32_e32 v153, 16, v153
	v_add3_u32 v175, v99, v175, s39
	v_and_or_b32 v153, v175, s38, v153
	v_pk_fma_f32 v[92:93], v[34:35], v[92:93], v[2:3]
	global_store_dwordx2 v[84:85], v[152:153], off
	v_med3_f32 v84, v92, s40, v172
	v_med3_f32 v85, v93, s40, v172
	v_mov_b32_e32 v152, 0
	v_cvt_pk_fp8_f32 v152, v84, v85
	v_pk_fma_f32 v[98:99], v[36:37], v[98:99], v[4:5]
	v_pk_mul_f32 v[100:101], v[100:101], v[90:91] op_sel_hi:[1,0]
	v_med3_f32 v84, v98, s40, v172
	v_med3_f32 v85, v99, s40, v172
	v_cvt_pk_fp8_f32 v152, v84, v85 op_sel:[0,0,1]
	v_lshl_add_u64 v[84:85], s[92:93], 0, v[66:67]
	v_add_co_u32_e32 v84, vcc, s41, v84
	v_pk_mul_f32 v[102:103], v[102:103], v[90:91] op_sel_hi:[1,0]
	s_nop 0
	v_addc_co_u32_e32 v85, vcc, 0, v85, vcc
	global_store_dword v[84:85], v152, off
	v_lshl_add_u64 v[152:153], v[70:71], 0, s[0:1]
	v_pk_mul_f32 v[104:105], v[104:105], v[90:91] op_sel_hi:[1,0]
	v_pk_mul_f32 v[106:107], v[106:107], v[90:91] op_sel_hi:[1,0]
	s_mov_b64 s[0:1], 0x34000400
	v_pk_mul_f32 v[94:95], v[94:95], v[90:91] op_sel_hi:[1,0]
	v_pk_mul_f32 v[96:97], v[96:97], v[90:91] op_sel_hi:[1,0]
	v_pk_mul_f32 v[86:87], v[86:87], v[90:91] op_sel_hi:[1,0]
	v_pk_mul_f32 v[88:89], v[88:89], v[90:91] op_sel_hi:[1,0]
	v_pk_mul_f32 v[80:81], v[80:81], v[90:91] op_sel_hi:[1,0]
	v_pk_mul_f32 v[82:83], v[82:83], v[90:91] op_sel_hi:[1,0]
	v_pk_mul_f32 v[72:73], v[72:73], v[90:91] op_sel_hi:[1,0]
	v_pk_mul_f32 v[74:75], v[74:75], v[90:91] op_sel_hi:[1,0]
	v_pk_mul_f32 v[184:185], v[76:77], v[90:91] op_sel_hi:[1,0]
	v_and_b32_sdwa v76, v98, v171 dst_sel:DWORD dst_unused:UNUSED_PAD src0_sel:WORD_1 src1_sel:DWORD
	v_and_b32_sdwa v77, v92, v171 dst_sel:DWORD dst_unused:UNUSED_PAD src0_sel:WORD_1 src1_sel:DWORD
	v_pk_mul_f32 v[186:187], v[78:79], v[90:91] op_sel_hi:[1,0]
	v_add3_u32 v90, v92, v77, s39
	v_add3_u32 v92, v98, v76, s39
	v_and_b32_sdwa v78, v99, v171 dst_sel:DWORD dst_unused:UNUSED_PAD src0_sel:WORD_1 src1_sel:DWORD
	v_add3_u32 v98, v99, v78, s39
	v_and_b32_sdwa v79, v93, v171 dst_sel:DWORD dst_unused:UNUSED_PAD src0_sel:WORD_1 src1_sel:DWORD
	v_add3_u32 v93, v93, v79, s39
	v_and_b32_e32 v98, 0xffff0000, v98
	v_and_b32_e32 v99, 0xffff0000, v93
	v_or_b32_sdwa v93, v98, v92 dst_sel:DWORD dst_unused:UNUSED_PAD src0_sel:DWORD src1_sel:WORD_1
	v_or_b32_sdwa v92, v99, v90 dst_sel:DWORD dst_unused:UNUSED_PAD src0_sel:DWORD src1_sel:WORD_1
	v_lshl_add_u64 v[66:67], v[66:67], 0, s[48:49]
	v_pk_fma_f32 v[100:101], v[214:215], v[100:101], v[250:251]
	v_pk_fma_f32 v[178:179], v[216:217], v[102:103], v[252:253]
	v_bfe_u32 v102, v100, 16, 1
	v_add3_u32 v102, v100, v102, s39
	v_bfe_u32 v103, v101, 16, 1
	v_lshrrev_b32_e32 v102, 16, v102
	v_add3_u32 v103, v101, v103, s39
	v_and_or_b32 v176, v103, s38, v102
	v_bfe_u32 v102, v178, 16, 1
	v_add3_u32 v102, v178, v102, s39
	v_pk_fma_f32 v[100:101], v[38:39], v[100:101], v[6:7]
	v_lshrrev_b32_e32 v175, 16, v102
	v_med3_f32 v102, v100, s40, v172
	v_med3_f32 v103, v101, s40, v172
	v_mov_b32_e32 v180, 0
	v_cvt_pk_fp8_f32 v180, v102, v103
	v_pk_fma_f32 v[102:103], v[40:41], v[178:179], v[8:9]
	v_bfe_u32 v177, v179, 16, 1
	v_med3_f32 v178, v102, s40, v172
	v_med3_f32 v181, v103, s40, v172
	v_cvt_pk_fp8_f32 v180, v178, v181 op_sel:[0,0,1]
	v_add3_u32 v177, v179, v177, s39
	v_and_or_b32 v177, v177, s38, v175
	global_store_dwordx2 v[152:153], v[176:177], off
	global_store_dword v[84:85], v180, off offset:256
	v_mov_b32_e32 v175, 0
	v_lshl_add_u64 v[152:153], v[70:71], 0, s[0:1]
	s_mov_b64 s[0:1], 0x34000600
	v_and_b32_sdwa v98, v100, v171 dst_sel:DWORD dst_unused:UNUSED_PAD src0_sel:WORD_1 src1_sel:DWORD
	v_and_b32_sdwa v99, v103, v171 dst_sel:DWORD dst_unused:UNUSED_PAD src0_sel:WORD_1 src1_sel:DWORD
	v_and_b32_sdwa v90, v102, v171 dst_sel:DWORD dst_unused:UNUSED_PAD src0_sel:WORD_1 src1_sel:DWORD
	v_add3_u32 v98, v100, v98, s39
	v_add3_u32 v99, v103, v99, s39
	v_add3_u32 v90, v102, v90, s39
	v_and_b32_e32 v99, 0xffff0000, v99
	v_or_b32_sdwa v99, v99, v90 dst_sel:DWORD dst_unused:UNUSED_PAD src0_sel:DWORD src1_sel:WORD_1
	v_pk_fma_f32 v[176:177], v[218:219], v[104:105], v[118:119]
	v_pk_fma_f32 v[178:179], v[220:221], v[106:107], v[120:121]
; #define GAS __attribute__((address_space(1)))
; #define LAS __attribute__((address_space(3)))
; __device__ __forceinline__ unsigned pk2(float lo, float hi) { return f2bf(lo) | (f2bf(hi) << 16); }
; __device__ __forceinline__ unsigned pk4_fp8(float a, float b, float c, float d) { int w = 0; w = __builtin_amdgcn_cvt_pk_fp8_f32(sat8(a), sat8(b), w, false); w = __builtin_amdgcn_cvt_pk_fp8_f32(sat8(c), sat8(d), w, true); return (unsigned)w; }
; __device__ __forceinline__ void phase_ln_router(const Frame& F, const Args& a, int layer) {
;     ...
;             for (int i = 0; i < 8; ++i) { const int c = 4 * F.lane + 256 * i;
;                 const f32x4 lat = v[i] * rstd * *(const GAS f32x4*)(lng + c) + *(const GAS f32x4*)(lnb + c);
;                 { u32x2 wl; wl.x = pk2(lat[0], lat[1]); wl.y = pk2(lat[2], lat[3]); *(GAS u32x2*)(xr + c) = wl; }
;                 const f32x4 h = lat * psc[i] + psh[i];
;                 u32x2 w; w.x = pk2(h[0], h[1]); w.y = pk2(h[2], h[3]); *(GAS unsigned*)((unsigned char*)A0 + (size_t)row * D + c) = pk4_fp8(h[0], h[1], h[2], h[3]);
;                 *(LAS u32x2*)(hb + j * HB_LD + c) = w; } }
	v_bfe_u32 v180, v176, 16, 1
	v_bfe_u32 v181, v177, 16, 1
	v_pk_fma_f32 v[106:107], v[42:43], v[176:177], v[10:11]
	v_add3_u32 v176, v176, v180, s39
	v_add3_u32 v177, v177, v181, s39
	v_med3_f32 v180, v106, s40, v172
	v_med3_f32 v181, v107, s40, v172
	v_cvt_pk_fp8_f32 v175, v180, v181
	v_bfe_u32 v182, v178, 16, 1
	v_pk_fma_f32 v[104:105], v[44:45], v[178:179], v[12:13]
	v_add3_u32 v178, v178, v182, s39
	v_med3_f32 v182, v104, s40, v172
	v_med3_f32 v180, v105, s40, v172
	v_bfe_u32 v183, v179, 16, 1
	v_cvt_pk_fp8_f32 v175, v182, v180 op_sel:[0,0,1]
	v_add3_u32 v179, v179, v183, s39
	v_lshrrev_b32_e32 v176, 16, v176
	v_lshrrev_b32_e32 v178, 16, v178
	v_and_or_b32 v176, v177, s38, v176
	v_and_or_b32 v177, v179, s38, v178
	global_store_dwordx2 v[152:153], v[176:177], off
	global_store_dword v[84:85], v175, off offset:512
	v_mov_b32_e32 v175, 0
	v_lshl_add_u64 v[152:153], v[70:71], 0, s[0:1]
	s_mov_b64 s[0:1], 0x34000800
	v_and_b32_sdwa v90, v104, v171 dst_sel:DWORD dst_unused:UNUSED_PAD src0_sel:WORD_1 src1_sel:DWORD
	v_add3_u32 v90, v104, v90, s39
	v_pk_fma_f32 v[176:177], v[222:223], v[94:95], v[122:123]
	v_pk_fma_f32 v[178:179], v[224:225], v[96:97], v[124:125]
	v_bfe_u32 v180, v176, 16, 1
	v_bfe_u32 v181, v177, 16, 1
	v_pk_fma_f32 v[96:97], v[46:47], v[176:177], v[14:15]
	v_add3_u32 v176, v176, v180, s39
	v_add3_u32 v177, v177, v181, s39
	v_med3_f32 v180, v96, s40, v172
	v_med3_f32 v181, v97, s40, v172
	v_cvt_pk_fp8_f32 v175, v180, v181
	v_bfe_u32 v182, v178, 16, 1
	v_pk_fma_f32 v[94:95], v[48:49], v[178:179], v[16:17]
	v_add3_u32 v178, v178, v182, s39
	v_med3_f32 v182, v94, s40, v172
	v_med3_f32 v180, v95, s40, v172
	v_bfe_u32 v183, v179, 16, 1
	v_cvt_pk_fp8_f32 v175, v182, v180 op_sel:[0,0,1]
	v_add3_u32 v179, v179, v183, s39
	v_lshrrev_b32_e32 v176, 16, v176
	v_lshrrev_b32_e32 v178, 16, v178
	v_and_or_b32 v176, v177, s38, v176
	v_and_or_b32 v177, v179, s38, v178
	global_store_dwordx2 v[152:153], v[176:177], off
	global_store_dword v[84:85], v175, off offset:768
	v_mov_b32_e32 v175, 0
	v_lshl_add_u64 v[152:153], v[70:71], 0, s[0:1]
	s_mov_b64 s[0:1], 0x34000a00
	v_pk_fma_f32 v[176:177], v[86:87], v[226:227], v[126:127]
	v_pk_fma_f32 v[178:179], v[88:89], v[228:229], v[128:129]
	v_bfe_u32 v180, v176, 16, 1
	v_bfe_u32 v181, v177, 16, 1
	v_pk_fma_f32 v[88:89], v[50:51], v[176:177], v[18:19]
	v_add3_u32 v176, v176, v180, s39
	v_add3_u32 v177, v177, v181, s39
	v_med3_f32 v180, v88, s40, v172
	v_med3_f32 v181, v89, s40, v172
	v_cvt_pk_fp8_f32 v175, v180, v181
	v_bfe_u32 v182, v178, 16, 1
	v_pk_fma_f32 v[86:87], v[52:53], v[178:179], v[20:21]
	v_add3_u32 v178, v178, v182, s39
	v_med3_f32 v182, v86, s40, v172
	v_med3_f32 v180, v87, s40, v172
	v_bfe_u32 v183, v179, 16, 1
	v_cvt_pk_fp8_f32 v175, v182, v180 op_sel:[0,0,1]
	v_add3_u32 v179, v179, v183, s39
	v_lshrrev_b32_e32 v176, 16, v176
	v_lshrrev_b32_e32 v178, 16, v178
	v_and_or_b32 v176, v177, s38, v176
	v_and_or_b32 v177, v179, s38, v178
	global_store_dwordx2 v[152:153], v[176:177], off
	global_store_dword v[84:85], v175, off offset:1024
	v_mov_b32_e32 v175, 0
	v_lshl_add_u64 v[152:153], v[70:71], 0, s[0:1]
	s_mov_b64 s[0:1], 0x34000c00
	v_pk_fma_f32 v[80:81], v[80:81], v[230:231], v[130:131]
	v_pk_fma_f32 v[82:83], v[82:83], v[232:233], v[132:133]
	v_bfe_u32 v176, v80, 16, 1
	v_bfe_u32 v177, v81, 16, 1
	v_pk_fma_f32 v[182:183], v[54:55], v[80:81], v[22:23]
	v_add3_u32 v80, v80, v176, s39
	v_add3_u32 v81, v81, v177, s39
	v_med3_f32 v176, v182, s40, v172
	v_med3_f32 v177, v183, s40, v172
	v_cvt_pk_fp8_f32 v175, v176, v177
	v_bfe_u32 v178, v82, 16, 1
	v_pk_fma_f32 v[180:181], v[56:57], v[82:83], v[24:25]
	v_add3_u32 v82, v82, v178, s39
	v_med3_f32 v178, v180, s40, v172
	v_med3_f32 v176, v181, s40, v172
	v_bfe_u32 v179, v83, 16, 1
	v_cvt_pk_fp8_f32 v175, v178, v176 op_sel:[0,0,1]
	v_add3_u32 v83, v83, v179, s39
	v_lshrrev_b32_e32 v80, 16, v80
	v_lshrrev_b32_e32 v82, 16, v82
	v_and_or_b32 v80, v81, s38, v80
	v_and_or_b32 v81, v83, s38, v82
	global_store_dwordx2 v[152:153], v[80:81], off
	global_store_dword v[84:85], v175, off offset:1280
	v_mov_b32_e32 v175, 0
	v_lshl_add_u64 v[152:153], v[70:71], 0, s[0:1]
	s_mov_b64 s[0:1], 0x34000e00
	v_lshl_add_u64 v[70:71], v[70:71], 0, s[0:1]
	s_mov_b64 s[0:1], 0x8000
	v_lshl_add_u64 v[68:69], v[68:69], 0, s[0:1]
	v_pk_fma_f32 v[72:73], v[72:73], v[234:235], v[134:135]
	v_pk_fma_f32 v[74:75], v[74:75], v[236:237], v[136:137]
	v_bfe_u32 v76, v72, 16, 1
	v_bfe_u32 v77, v73, 16, 1
	v_pk_fma_f32 v[82:83], v[58:59], v[72:73], v[26:27]
	v_add3_u32 v72, v72, v76, s39
	v_add3_u32 v73, v73, v77, s39
	v_med3_f32 v76, v82, s40, v172
	v_med3_f32 v77, v83, s40, v172
	v_cvt_pk_fp8_f32 v175, v76, v77
	v_bfe_u32 v78, v74, 16, 1
	v_pk_fma_f32 v[80:81], v[60:61], v[74:75], v[28:29]
	v_add3_u32 v74, v74, v78, s39
	v_med3_f32 v78, v80, s40, v172
	v_med3_f32 v76, v81, s40, v172
	v_bfe_u32 v79, v75, 16, 1
	v_cvt_pk_fp8_f32 v175, v78, v76 op_sel:[0,0,1]
	v_add3_u32 v75, v75, v79, s39
	v_lshrrev_b32_e32 v72, 16, v72
	v_lshrrev_b32_e32 v74, 16, v74
	v_and_or_b32 v72, v73, s38, v72
	v_and_or_b32 v73, v75, s38, v74
	global_store_dwordx2 v[152:153], v[72:73], off
	global_store_dword v[84:85], v175, off offset:1536
	v_and_b32_sdwa v152, v101, v171 dst_sel:DWORD dst_unused:UNUSED_PAD src0_sel:WORD_1 src1_sel:DWORD
	v_add3_u32 v100, v101, v152, s39
	v_and_b32_e32 v100, 0xffff0000, v100
	v_or_b32_sdwa v98, v100, v98 dst_sel:DWORD dst_unused:UNUSED_PAD src0_sel:DWORD src1_sel:WORD_1
	ds_write2st64_b64 v113, v[92:93], v[98:99] offset1:1
	v_and_b32_sdwa v93, v105, v171 dst_sel:DWORD dst_unused:UNUSED_PAD src0_sel:WORD_1 src1_sel:DWORD
; #define GAS __attribute__((address_space(1)))
; #define LAS __attribute__((address_space(3)))
; __device__ __forceinline__ unsigned pk2(float lo, float hi) { return f2bf(lo) | (f2bf(hi) << 16); }
; __device__ __forceinline__ unsigned pk4_fp8(float a, float b, float c, float d) { int w = 0; w = __builtin_amdgcn_cvt_pk_fp8_f32(sat8(a), sat8(b), w, false); w = __builtin_amdgcn_cvt_pk_fp8_f32(sat8(c), sat8(d), w, true); return (unsigned)w; }
; __device__ __forceinline__ void phase_ln_router(const Frame& F, const Args& a, int layer) {
;     ...
;             for (int i = 0; i < 8; ++i) { const int c = 4 * F.lane + 256 * i;
;                 const f32x4 lat = v[i] * rstd * *(const GAS f32x4*)(lng + c) + *(const GAS f32x4*)(lnb + c);
;                 { u32x2 wl; wl.x = pk2(lat[0], lat[1]); wl.y = pk2(lat[2], lat[3]); *(GAS u32x2*)(xr + c) = wl; }
;                 const f32x4 h = lat * psc[i] + psh[i];
;                 u32x2 w; w.x = pk2(h[0], h[1]); w.y = pk2(h[2], h[3]); *(GAS unsigned*)((unsigned char*)A0 + (size_t)row * D + c) = pk4_fp8(h[0], h[1], h[2], h[3]);
;                 *(LAS u32x2*)(hb + j * HB_LD + c) = w; } }
	v_and_b32_sdwa v98, v107, v171 dst_sel:DWORD dst_unused:UNUSED_PAD src0_sel:WORD_1 src1_sel:DWORD
	v_add3_u32 v93, v105, v93, s39
	v_and_b32_sdwa v92, v106, v171 dst_sel:DWORD dst_unused:UNUSED_PAD src0_sel:WORD_1 src1_sel:DWORD
	v_add3_u32 v98, v107, v98, s39
	v_and_b32_e32 v93, 0xffff0000, v93
	v_add3_u32 v92, v106, v92, s39
	v_and_b32_e32 v98, 0xffff0000, v98
	v_or_b32_sdwa v93, v93, v90 dst_sel:DWORD dst_unused:UNUSED_PAD src0_sel:DWORD src1_sel:WORD_1
	v_and_b32_sdwa v90, v94, v171 dst_sel:DWORD dst_unused:UNUSED_PAD src0_sel:WORD_1 src1_sel:DWORD
	v_and_b32_sdwa v99, v95, v171 dst_sel:DWORD dst_unused:UNUSED_PAD src0_sel:WORD_1 src1_sel:DWORD
	v_and_b32_sdwa v100, v97, v171 dst_sel:DWORD dst_unused:UNUSED_PAD src0_sel:WORD_1 src1_sel:DWORD
	v_or_b32_sdwa v92, v98, v92 dst_sel:DWORD dst_unused:UNUSED_PAD src0_sel:DWORD src1_sel:WORD_1
	v_and_b32_sdwa v98, v96, v171 dst_sel:DWORD dst_unused:UNUSED_PAD src0_sel:WORD_1 src1_sel:DWORD
	v_add3_u32 v90, v94, v90, s39
	v_add3_u32 v94, v95, v99, s39
	v_add3_u32 v95, v97, v100, s39
	v_add3_u32 v96, v96, v98, s39
	v_and_b32_e32 v94, 0xffff0000, v94
	v_and_b32_e32 v97, 0xffff0000, v95
	v_or_b32_sdwa v95, v94, v90 dst_sel:DWORD dst_unused:UNUSED_PAD src0_sel:DWORD src1_sel:WORD_1
	v_or_b32_sdwa v94, v97, v96 dst_sel:DWORD dst_unused:UNUSED_PAD src0_sel:DWORD src1_sel:WORD_1
	ds_write2st64_b64 v113, v[92:93], v[94:95] offset0:2 offset1:3
	v_and_b32_sdwa v93, v87, v171 dst_sel:DWORD dst_unused:UNUSED_PAD src0_sel:WORD_1 src1_sel:DWORD
	v_and_b32_sdwa v94, v89, v171 dst_sel:DWORD dst_unused:UNUSED_PAD src0_sel:WORD_1 src1_sel:DWORD
	v_and_b32_sdwa v90, v86, v171 dst_sel:DWORD dst_unused:UNUSED_PAD src0_sel:WORD_1 src1_sel:DWORD
	v_and_b32_sdwa v92, v88, v171 dst_sel:DWORD dst_unused:UNUSED_PAD src0_sel:WORD_1 src1_sel:DWORD
	v_add3_u32 v87, v87, v93, s39
	v_add3_u32 v89, v89, v94, s39
	v_add3_u32 v88, v88, v92, s39
	v_add3_u32 v86, v86, v90, s39
	v_and_b32_e32 v87, 0xffff0000, v87
	v_and_b32_e32 v89, 0xffff0000, v89
	v_or_b32_sdwa v87, v87, v86 dst_sel:DWORD dst_unused:UNUSED_PAD src0_sel:DWORD src1_sel:WORD_1
	v_or_b32_sdwa v86, v89, v88 dst_sel:DWORD dst_unused:UNUSED_PAD src0_sel:DWORD src1_sel:WORD_1
	v_and_b32_sdwa v89, v182, v171 dst_sel:DWORD dst_unused:UNUSED_PAD src0_sel:WORD_1 src1_sel:DWORD
	v_and_b32_sdwa v90, v181, v171 dst_sel:DWORD dst_unused:UNUSED_PAD src0_sel:WORD_1 src1_sel:DWORD
	v_and_b32_sdwa v92, v183, v171 dst_sel:DWORD dst_unused:UNUSED_PAD src0_sel:WORD_1 src1_sel:DWORD
	v_and_b32_sdwa v88, v180, v171 dst_sel:DWORD dst_unused:UNUSED_PAD src0_sel:WORD_1 src1_sel:DWORD
	v_add3_u32 v93, v182, v89, s39
	v_add3_u32 v89, v181, v90, s39
	v_add3_u32 v90, v183, v92, s39
	v_add3_u32 v88, v180, v88, s39
	v_and_b32_e32 v89, 0xffff0000, v89
	v_and_b32_e32 v90, 0xffff0000, v90
	v_or_b32_sdwa v89, v89, v88 dst_sel:DWORD dst_unused:UNUSED_PAD src0_sel:DWORD src1_sel:WORD_1
	v_or_b32_sdwa v88, v90, v93 dst_sel:DWORD dst_unused:UNUSED_PAD src0_sel:DWORD src1_sel:WORD_1
	ds_write2st64_b64 v113, v[86:87], v[88:89] offset0:4 offset1:5
	v_and_b32_sdwa v88, v81, v171 dst_sel:DWORD dst_unused:UNUSED_PAD src0_sel:WORD_1 src1_sel:DWORD
	v_and_b32_sdwa v89, v83, v171 dst_sel:DWORD dst_unused:UNUSED_PAD src0_sel:WORD_1 src1_sel:DWORD
	v_add3_u32 v81, v81, v88, s39
	v_add3_u32 v83, v83, v89, s39
	v_and_b32_sdwa v86, v80, v171 dst_sel:DWORD dst_unused:UNUSED_PAD src0_sel:WORD_1 src1_sel:DWORD
	v_and_b32_sdwa v87, v82, v171 dst_sel:DWORD dst_unused:UNUSED_PAD src0_sel:WORD_1 src1_sel:DWORD
	v_add3_u32 v82, v82, v87, s39
	v_add3_u32 v80, v80, v86, s39
	v_and_b32_e32 v81, 0xffff0000, v81
	v_and_b32_e32 v83, 0xffff0000, v83
	v_or_b32_sdwa v81, v81, v80 dst_sel:DWORD dst_unused:UNUSED_PAD src0_sel:DWORD src1_sel:WORD_1
	v_or_b32_sdwa v80, v83, v82 dst_sel:DWORD dst_unused:UNUSED_PAD src0_sel:DWORD src1_sel:WORD_1
	v_pk_fma_f32 v[72:73], v[184:185], v[238:239], v[138:139]
	v_pk_fma_f32 v[74:75], v[186:187], v[240:241], v[140:141]
	v_pk_fma_f32 v[78:79], v[62:63], v[72:73], v[30:31]
	v_bfe_u32 v82, v72, 16, 1
	v_med3_f32 v88, v78, s40, v172
	v_med3_f32 v89, v79, s40, v172
	v_cvt_pk_fp8_f32 v188, v88, v89
	v_bfe_u32 v86, v74, 16, 1
	v_bfe_u32 v87, v75, 16, 1
	v_pk_fma_f32 v[76:77], v[64:65], v[74:75], v[32:33]
	v_bfe_u32 v83, v73, 16, 1
	v_add3_u32 v72, v72, v82, s39
	v_add3_u32 v74, v74, v86, s39
	v_add3_u32 v75, v75, v87, s39
	v_and_b32_sdwa v86, v77, v171 dst_sel:DWORD dst_unused:UNUSED_PAD src0_sel:WORD_1 src1_sel:DWORD
	v_and_b32_sdwa v87, v79, v171 dst_sel:DWORD dst_unused:UNUSED_PAD src0_sel:WORD_1 src1_sel:DWORD
	v_med3_f32 v90, v76, s40, v172
	v_med3_f32 v92, v77, s40, v172
	v_add3_u32 v73, v73, v83, s39
	v_and_b32_sdwa v82, v76, v171 dst_sel:DWORD dst_unused:UNUSED_PAD src0_sel:WORD_1 src1_sel:DWORD
	v_and_b32_sdwa v83, v78, v171 dst_sel:DWORD dst_unused:UNUSED_PAD src0_sel:WORD_1 src1_sel:DWORD
	v_lshrrev_b32_e32 v72, 16, v72
	v_lshrrev_b32_e32 v74, 16, v74
	v_add3_u32 v77, v77, v86, s39
	v_add3_u32 v79, v79, v87, s39
	v_cvt_pk_fp8_f32 v188, v90, v92 op_sel:[0,0,1]
	v_add3_u32 v78, v78, v83, s39
	v_add3_u32 v76, v76, v82, s39
	v_and_or_b32 v72, v73, s38, v72
	v_and_or_b32 v73, v75, s38, v74
	v_and_b32_e32 v74, 0xffff0000, v77
	v_and_b32_e32 v75, 0xffff0000, v79
	global_store_dwordx2 v[70:71], v[72:73], off
	v_or_b32_sdwa v71, v74, v76 dst_sel:DWORD dst_unused:UNUSED_PAD src0_sel:DWORD src1_sel:WORD_1
	v_or_b32_sdwa v70, v75, v78 dst_sel:DWORD dst_unused:UNUSED_PAD src0_sel:DWORD src1_sel:WORD_1
	ds_write2st64_b64 v113, v[80:81], v[70:71] offset0:6 offset1:7
	v_add_u32_e32 v113, 0x8080, v113
	global_store_dword v[84:85], v188, off offset:1792
	s_cbranch_scc1 .LBB0_3038
	s_mov_b32 s30, s22
	s_branch .LBB0_3034

; __device__ __forceinline__ void phase_ln_router(const Frame& F, const Args& a, int layer) {
;     ...
;             const bool sel = gsel && rank < TOPK;
;             const float wsum = wave_sum(sel ? sg : 0.f);
;             if (sel) { SE[row * 8 + rank] = F.lane; SW[row * 8 + rank] = sg / wsum * 2.5f; mycnt += 1; } }
.LBB0_3076:
	v_cmp_gt_u32_e64 s[0:1], 8, v74
	s_and_b64 vcc, vcc, s[0:1]
	v_cndmask_b32_e32 v75, 0, v73, vcc
	s_waitcnt lgkmcnt(0)
	s_nop 1
	v_add_f32_dpp v75, v75, v75 quad_perm:[1,0,3,2] row_mask:0xf bank_mask:0xf
	s_waitcnt lgkmcnt(0)
	s_nop 1
	v_add_f32_dpp v75, v75, v75 quad_perm:[2,3,0,1] row_mask:0xf bank_mask:0xf
	s_waitcnt lgkmcnt(0)
	s_nop 1
	v_add_f32_dpp v75, v75, v75 row_half_mirror row_mask:0xf bank_mask:0xf
	s_waitcnt lgkmcnt(0)
	s_nop 1
	v_add_f32_dpp v75, v75, v75 row_mirror row_mask:0xf bank_mask:0xf
	v_mov_b32_e32 v76, v75
	s_nop 1
	v_permlane16_swap_b32 v76, v75
	s_waitcnt lgkmcnt(0)
	v_add_f32_e32 v75, v75, v76
	v_mov_b32_e32 v76, v75
	s_nop 1
	v_permlane32_swap_b32 v76, v75
	s_and_saveexec_b64 s[0:1], vcc
	s_cbranch_execz .LBB0_3078
	s_add_i32 s28, s22, s2
	s_waitcnt lgkmcnt(0)
	v_add_f32_e32 v78, v75, v76
	v_lshl_or_b32 v74, s28, 3, v74
	v_div_scale_f32 v79, s[28:29], v78, v78, v73
	v_rcp_f32_e32 v80, v79
	v_ashrrev_i32_e32 v75, 31, v74
	v_lshlrev_b64 v[74:75], 2, v[74:75]
	v_lshl_add_u64 v[76:77], s[24:25], 0, v[74:75]
	global_store_dword v[76:77], v1, off
	v_fma_f32 v76, -v79, v80, 1.0
	v_fmac_f32_e32 v80, v76, v80
	v_div_scale_f32 v76, vcc, v73, v78, v73
	v_mul_f32_e32 v77, v76, v80
	v_fma_f32 v81, -v79, v77, v76
	v_fmac_f32_e32 v77, v81, v80
	v_fma_f32 v76, -v79, v77, v76
	v_div_fmas_f32 v76, v76, v80, v77
	v_div_fixup_f32 v73, v76, v78, v73
	v_mul_f32_e32 v73, 0x40200000, v73
	v_lshl_add_u64 v[74:75], s[26:27], 0, v[74:75]
	v_add_u32_e32 v66, 1, v66
	global_store_dword v[74:75], v73, off

; #define GAS __attribute__((address_space(1)))
; __device__ __forceinline__ f32x4 up4_fp8(unsigned w) { const f32x2 lo = __builtin_amdgcn_cvt_pk_f32_fp8((int)w, false), hi = __builtin_amdgcn_cvt_pk_f32_fp8((int)w, true); return (f32x4){lo[0], lo[1], hi[0], hi[1]}; }
; __device__ __forceinline__ void phase_combine(const Frame& F, const Args& a, int layer) {
;     ...
;             for (int jj = 0; jj < 8; ++jj) { const int slot = TOK_SLOT[row * 8 + jj]; const float w = SW[row * 8 + jj] * 0.0625f; const unsigned char* ys = YS + (size_t)slot * D;
; #pragma unroll
;                 for (int i = 0; i < 8; ++i) f[i] += up4_fp8(*(const GAS unsigned*)(ys + 4 * F.lane + 256 * i)) * w; }
.LBB0_3532:
	s_add_i32 s10, s19, s9
	s_addk_i32 s10, 0x1008
	s_ashr_i32 s11, s10, 31
	s_lshl_b64 s[10:11], s[10:11], 2
	s_add_u32 s22, s7, s10
	s_addc_u32 s23, s12, s11
	global_load_dwordx2 v[102:103], v65, s[22:23]
	s_add_u32 s10, s2, s10
	s_addc_u32 s11, s5, s11
	global_load_dwordx2 v[104:105], v65, s[10:11]
	s_add_i32 s9, s9, 2
	s_cmp_eq_u32 s9, 0
	s_waitcnt vmcnt(1)
	v_ashrrev_i32_e32 v127, 31, v102
	v_mov_b32_e32 v126, v102
	v_ashrrev_i32_e32 v129, 31, v103
	v_mov_b32_e32 v128, v103
	v_lshlrev_b64 v[102:103], 11, v[126:127]
	v_lshlrev_b64 v[126:127], 11, v[128:129]
	v_lshl_add_u64 v[102:103], v[66:67], 0, v[102:103]
	v_lshl_add_u64 v[126:127], v[66:67], 0, v[126:127]
	global_load_dword v128, v[102:103], off
	global_load_dword v132, v[102:103], off offset:256
	global_load_dword v136, v[102:103], off offset:512
	global_load_dword v140, v[102:103], off offset:768
	global_load_dword v144, v[102:103], off offset:1024
	global_load_dword v148, v[102:103], off offset:1280
	global_load_dword v152, v[102:103], off offset:1536
	s_nop 0
	global_load_dword v103, v[102:103], off offset:1792
	s_nop 0
	global_load_dword v160, v[126:127], off
	global_load_dword v164, v[126:127], off offset:256
	global_load_dword v168, v[126:127], off offset:512
	global_load_dword v172, v[126:127], off offset:768
	global_load_dword v176, v[126:127], off offset:1024
	global_load_dword v180, v[126:127], off offset:1280
	global_load_dword v184, v[126:127], off offset:1536
	global_load_dword v188, v[126:127], off offset:1792
	s_waitcnt vmcnt(16)
	v_mul_f32_e32 v102, 0x3d800000, v104
	v_mul_f32_e32 v104, 0x3d800000, v105
	s_waitcnt vmcnt(15)
	v_cvt_pk_f32_fp8_e32 v[126:127], v128
	v_cvt_pk_f32_fp8_sdwa v[128:129], v128 src0_sel:WORD_1
	s_waitcnt vmcnt(14)
	v_cvt_pk_f32_fp8_e32 v[130:131], v132
	v_cvt_pk_f32_fp8_sdwa v[132:133], v132 src0_sel:WORD_1
	s_waitcnt vmcnt(13)
	v_cvt_pk_f32_fp8_e32 v[134:135], v136
	v_cvt_pk_f32_fp8_sdwa v[136:137], v136 src0_sel:WORD_1
	s_waitcnt vmcnt(12)
	v_cvt_pk_f32_fp8_e32 v[138:139], v140
	v_cvt_pk_f32_fp8_sdwa v[140:141], v140 src0_sel:WORD_1
	s_waitcnt vmcnt(11)
	v_cvt_pk_f32_fp8_e32 v[142:143], v144
	v_cvt_pk_f32_fp8_sdwa v[144:145], v144 src0_sel:WORD_1
	s_waitcnt vmcnt(10)
	v_cvt_pk_f32_fp8_e32 v[146:147], v148
	v_cvt_pk_f32_fp8_sdwa v[148:149], v148 src0_sel:WORD_1
	s_waitcnt vmcnt(9)
	v_cvt_pk_f32_fp8_e32 v[150:151], v152
	v_cvt_pk_f32_fp8_sdwa v[152:153], v152 src0_sel:WORD_1
	s_waitcnt vmcnt(8)
	v_cvt_pk_f32_fp8_e32 v[154:155], v103
	v_cvt_pk_f32_fp8_sdwa v[156:157], v103 src0_sel:WORD_1
	s_waitcnt vmcnt(7)
	v_cvt_pk_f32_fp8_e32 v[158:159], v160
	v_cvt_pk_f32_fp8_sdwa v[160:161], v160 src0_sel:WORD_1
	s_waitcnt vmcnt(6)
	v_cvt_pk_f32_fp8_e32 v[162:163], v164
	v_cvt_pk_f32_fp8_sdwa v[164:165], v164 src0_sel:WORD_1
	s_waitcnt vmcnt(5)
	v_cvt_pk_f32_fp8_e32 v[166:167], v168
	v_cvt_pk_f32_fp8_sdwa v[168:169], v168 src0_sel:WORD_1
	s_waitcnt vmcnt(4)
	v_cvt_pk_f32_fp8_e32 v[170:171], v172
	v_cvt_pk_f32_fp8_sdwa v[172:173], v172 src0_sel:WORD_1
	s_waitcnt vmcnt(3)
	v_cvt_pk_f32_fp8_e32 v[174:175], v176
	v_cvt_pk_f32_fp8_sdwa v[176:177], v176 src0_sel:WORD_1
	s_waitcnt vmcnt(2)
	v_cvt_pk_f32_fp8_e32 v[178:179], v180
	v_cvt_pk_f32_fp8_sdwa v[180:181], v180 src0_sel:WORD_1
	s_waitcnt vmcnt(1)
	v_cvt_pk_f32_fp8_e32 v[182:183], v184
	v_cvt_pk_f32_fp8_sdwa v[184:185], v184 src0_sel:WORD_1
	s_waitcnt vmcnt(0)
	v_cvt_pk_f32_fp8_e32 v[186:187], v188
	v_cvt_pk_f32_fp8_sdwa v[188:189], v188 src0_sel:WORD_1
	v_pk_fma_f32 v[100:101], v[102:103], v[126:127], v[100:101] op_sel_hi:[0,1,1]
	v_pk_fma_f32 v[90:91], v[102:103], v[128:129], v[90:91] op_sel_hi:[0,1,1]
	v_pk_fma_f32 v[98:99], v[102:103], v[130:131], v[98:99] op_sel_hi:[0,1,1]
	v_pk_fma_f32 v[88:89], v[102:103], v[132:133], v[88:89] op_sel_hi:[0,1,1]
	v_pk_fma_f32 v[96:97], v[102:103], v[134:135], v[96:97] op_sel_hi:[0,1,1]
	v_pk_fma_f32 v[86:87], v[102:103], v[136:137], v[86:87] op_sel_hi:[0,1,1]
	v_pk_fma_f32 v[94:95], v[102:103], v[138:139], v[94:95] op_sel_hi:[0,1,1]
	v_pk_fma_f32 v[84:85], v[102:103], v[140:141], v[84:85] op_sel_hi:[0,1,1]
	v_pk_fma_f32 v[92:93], v[102:103], v[142:143], v[92:93] op_sel_hi:[0,1,1]
	v_pk_fma_f32 v[82:83], v[102:103], v[144:145], v[82:83] op_sel_hi:[0,1,1]
	v_pk_fma_f32 v[80:81], v[102:103], v[146:147], v[80:81] op_sel_hi:[0,1,1]
	v_pk_fma_f32 v[78:79], v[102:103], v[148:149], v[78:79] op_sel_hi:[0,1,1]
	v_pk_fma_f32 v[76:77], v[102:103], v[150:151], v[76:77] op_sel_hi:[0,1,1]
	v_pk_fma_f32 v[74:75], v[102:103], v[152:153], v[74:75] op_sel_hi:[0,1,1]
	v_pk_fma_f32 v[72:73], v[102:103], v[154:155], v[72:73] op_sel_hi:[0,1,1]
	v_pk_fma_f32 v[70:71], v[102:103], v[156:157], v[70:71] op_sel_hi:[0,1,1]
	v_pk_fma_f32 v[90:91], v[104:105], v[160:161], v[90:91] op_sel_hi:[0,1,1]
	v_pk_fma_f32 v[100:101], v[104:105], v[158:159], v[100:101] op_sel_hi:[0,1,1]
	v_pk_fma_f32 v[88:89], v[104:105], v[164:165], v[88:89] op_sel_hi:[0,1,1]
	v_pk_fma_f32 v[98:99], v[104:105], v[162:163], v[98:99] op_sel_hi:[0,1,1]
	v_pk_fma_f32 v[86:87], v[104:105], v[168:169], v[86:87] op_sel_hi:[0,1,1]
	v_pk_fma_f32 v[96:97], v[104:105], v[166:167], v[96:97] op_sel_hi:[0,1,1]
	v_pk_fma_f32 v[84:85], v[104:105], v[172:173], v[84:85] op_sel_hi:[0,1,1]
	v_pk_fma_f32 v[94:95], v[104:105], v[170:171], v[94:95] op_sel_hi:[0,1,1]
	v_pk_fma_f32 v[82:83], v[104:105], v[176:177], v[82:83] op_sel_hi:[0,1,1]
	v_pk_fma_f32 v[92:93], v[104:105], v[174:175], v[92:93] op_sel_hi:[0,1,1]
	v_pk_fma_f32 v[78:79], v[104:105], v[180:181], v[78:79] op_sel_hi:[0,1,1]
	v_pk_fma_f32 v[80:81], v[104:105], v[178:179], v[80:81] op_sel_hi:[0,1,1]
	v_pk_fma_f32 v[74:75], v[104:105], v[184:185], v[74:75] op_sel_hi:[0,1,1]
	v_pk_fma_f32 v[76:77], v[104:105], v[182:183], v[76:77] op_sel_hi:[0,1,1]
	v_pk_fma_f32 v[70:71], v[104:105], v[188:189], v[70:71] op_sel_hi:[0,1,1]
	v_pk_fma_f32 v[72:73], v[104:105], v[186:187], v[72:73] op_sel_hi:[0,1,1]
	s_cbranch_scc0 .LBB0_3532
; #define GAS __attribute__((address_space(1)))
; #define LAS __attribute__((address_space(3)))
; __device__ __forceinline__ void phase_combine(const Frame& F, const Args& a, int layer) {
;     ...
;             const int r = modrow(row); bf16_t* xr = X + (size_t)row * D; float s = 0.f;
;             const LAS float* pg2 = P + (2 + 3 * r) * D;
; #pragma unroll
;             for (int i = 0; i < 8; ++i) { const int c = 4 * F.lane + 256 * i; const u32x2 p = *(const GAS u32x2*)(xr + c); const f32x4 xv = {bflo(p.x), bfhi(p.x), bflo(p.y), bfhi(p.y)};
;                 f[i] = xv * ALPHA + *(const LAS f32x4*)(pg2 + c) * f[i]; s += (f[i][0] + f[i][1]) + (f[i][2] + f[i][3]); }
	s_ashr_i32 s9, s8, 31
	s_lshl_b64 s[10:11], s[8:9], 12
	v_lshl_add_u64 v[102:103], v[68:69], 0, s[10:11]
	global_load_dwordx2 v[104:105], v[102:103], off
	global_load_dwordx2 v[150:151], v[102:103], off offset:512
	global_load_dwordx2 v[152:153], v[102:103], off offset:1024
	global_load_dwordx2 v[154:155], v[102:103], off offset:1536
	global_load_dwordx2 v[156:157], v[102:103], off offset:2048
	global_load_dwordx2 v[158:159], v[102:103], off offset:2560
	global_load_dwordx2 v[160:161], v[102:103], off offset:3072
	global_load_dwordx2 v[162:163], v[102:103], off offset:3584
	s_add_i32 s10, s20, s17
	s_lshr_b32 s9, s10, 12
	s_mulk_i32 s9, 0x6000
	s_cmpk_gt_i32 s8, 0x1ff
	s_cselect_b32 s8, s9, 0xc000
	v_add_u32_e32 v176, s8, v106
	ds_read_b128 v[126:129], v176 offset:16384
	ds_read_b128 v[130:133], v176 offset:17408
	ds_read_b128 v[134:137], v176 offset:18432
	ds_read_b128 v[138:141], v176 offset:19456
	ds_read_b128 v[142:145], v176 offset:20480
	ds_read_b128 v[146:149], v176 offset:21504
	s_ashr_i32 s11, s10, 31
	s_lshl_b64 s[8:9], s[10:11], 13
	s_add_u32 s8, s90, s8
	s_addc_u32 s9, s91, s9
	s_add_i32 s19, s19, 64
	s_waitcnt vmcnt(7)
	v_lshlrev_b32_e32 v102, 16, v104
	v_and_b32_e32 v103, 0xffff0000, v104
	v_lshlrev_b32_e32 v104, 16, v105
	v_and_b32_e32 v105, 0xffff0000, v105
	s_waitcnt vmcnt(6)
	v_lshlrev_b32_e32 v164, 16, v150
	v_and_b32_e32 v165, 0xffff0000, v150
	v_lshlrev_b32_e32 v150, 16, v151
	v_and_b32_e32 v151, 0xffff0000, v151
	s_waitcnt vmcnt(5)
	v_lshlrev_b32_e32 v166, 16, v152
	v_and_b32_e32 v167, 0xffff0000, v152
	v_lshlrev_b32_e32 v152, 16, v153
	v_and_b32_e32 v153, 0xffff0000, v153
	s_waitcnt vmcnt(4)
	v_lshlrev_b32_e32 v168, 16, v154
	v_and_b32_e32 v169, 0xffff0000, v154
	v_lshlrev_b32_e32 v154, 16, v155
	v_and_b32_e32 v155, 0xffff0000, v155
	s_waitcnt vmcnt(3)
	v_lshlrev_b32_e32 v170, 16, v156
	v_and_b32_e32 v171, 0xffff0000, v156
	v_pk_mul_f32 v[174:175], v[102:103], s[6:7] op_sel_hi:[1,0]
	v_pk_mul_f32 v[102:103], v[104:105], s[6:7] op_sel_hi:[1,0]
	v_pk_mul_f32 v[164:165], v[164:165], s[6:7] op_sel_hi:[1,0]
	v_pk_mul_f32 v[150:151], v[150:151], s[6:7] op_sel_hi:[1,0]
	v_pk_mul_f32 v[166:167], v[166:167], s[6:7] op_sel_hi:[1,0]
	v_pk_mul_f32 v[152:153], v[152:153], s[6:7] op_sel_hi:[1,0]
	v_pk_mul_f32 v[168:169], v[168:169], s[6:7] op_sel_hi:[1,0]
	v_pk_mul_f32 v[154:155], v[154:155], s[6:7] op_sel_hi:[1,0]
	v_pk_mul_f32 v[170:171], v[170:171], s[6:7] op_sel_hi:[1,0]
	s_waitcnt lgkmcnt(5)
	v_pk_fma_f32 v[102:103], v[90:91], v[128:129], v[102:103]
	v_pk_fma_f32 v[104:105], v[100:101], v[126:127], v[174:175]
	s_waitcnt lgkmcnt(4)
	v_pk_fma_f32 v[100:101], v[88:89], v[132:133], v[150:151]
	v_pk_fma_f32 v[98:99], v[98:99], v[130:131], v[164:165]
	s_waitcnt lgkmcnt(3)
	v_pk_fma_f32 v[90:91], v[86:87], v[136:137], v[152:153]
	v_pk_fma_f32 v[96:97], v[96:97], v[134:135], v[166:167]
	s_waitcnt lgkmcnt(2)
	v_pk_fma_f32 v[86:87], v[84:85], v[140:141], v[154:155]
	v_pk_fma_f32 v[88:89], v[94:95], v[138:139], v[168:169]
	s_waitcnt lgkmcnt(1)
	v_pk_fma_f32 v[84:85], v[92:93], v[142:143], v[170:171]
	v_mov_b32_e32 v92, v104
	v_mov_b32_e32 v93, v98
	v_mov_b32_e32 v94, v105
	v_mov_b32_e32 v95, v99
	v_mov_b32_e32 v126, v102
	v_mov_b32_e32 v127, v100
	v_mov_b32_e32 v128, v103
	v_mov_b32_e32 v129, v101
	v_lshlrev_b32_e32 v156, 16, v157
	v_and_b32_e32 v157, 0xffff0000, v157
	v_pk_mov_b32 v[130:131], v[96:97], v[90:91] op_sel:[1,0]
	v_mov_b32_e32 v132, v96
	v_mov_b32_e32 v133, v91
	v_pk_add_f32 v[92:93], v[92:93], v[94:95]
	v_pk_add_f32 v[94:95], v[126:127], v[128:129]
	v_pk_mul_f32 v[156:157], v[156:157], s[6:7] op_sel_hi:[1,0]
	v_pk_add_f32 v[126:127], v[130:131], v[132:133]
	v_pk_add_f32 v[92:93], v[92:93], v[94:95]
	v_pk_fma_f32 v[82:83], v[82:83], v[144:145], v[156:157]
	v_pk_add_f32 v[94:95], v[126:127], v[126:127] op_sel:[0,1] op_sel_hi:[1,0]
	v_add_f32_e32 v92, 0, v92
	v_add_f32_e32 v134, v88, v89
	v_add_f32_e32 v136, v86, v87
	v_mov_b32_e32 v139, v84
	v_mov_b32_e32 v135, v82
	v_mov_b32_e32 v137, v83
	v_mov_b32_e32 v95, v85
	v_add_f32_e32 v138, v92, v93
	v_pk_add_f32 v[128:129], v[134:135], v[136:137]
	v_pk_add_f32 v[92:93], v[138:139], v[94:95]
	s_waitcnt vmcnt(2)
	v_lshlrev_b32_e32 v172, 16, v158
	v_and_b32_e32 v173, 0xffff0000, v158
	v_lshlrev_b32_e32 v158, 16, v159
	v_pk_add_f32 v[92:93], v[92:93], v[128:129]
	v_and_b32_e32 v159, 0xffff0000, v159
	v_pk_add_f32 v[130:131], v[92:93], v[92:93] op_sel:[0,1] op_sel_hi:[1,0]
	v_pk_mul_f32 v[92:93], v[172:173], s[6:7] op_sel_hi:[1,0]
	v_pk_mul_f32 v[94:95], v[158:159], s[6:7] op_sel_hi:[1,0]
	s_waitcnt lgkmcnt(0)
	v_pk_fma_f32 v[80:81], v[80:81], v[146:147], v[92:93]
	v_pk_fma_f32 v[78:79], v[78:79], v[148:149], v[94:95]
	v_mov_b32_e32 v94, v80
	v_pk_mov_b32 v[92:93], v[80:81], v[78:79] op_sel:[1,0]
	v_mov_b32_e32 v95, v79
	v_pk_add_f32 v[92:93], v[92:93], v[94:95]
	s_waitcnt vmcnt(1)
	v_lshlrev_b32_e32 v126, 16, v160
	v_pk_add_f32 v[132:133], v[92:93], v[92:93] op_sel:[0,1] op_sel_hi:[1,0]
	ds_read_b128 v[92:95], v176 offset:22528
	v_and_b32_e32 v127, 0xffff0000, v160
	v_lshlrev_b32_e32 v128, 16, v161
	v_and_b32_e32 v129, 0xffff0000, v161
	v_pk_mul_f32 v[134:135], v[126:127], s[6:7] op_sel_hi:[1,0]
	v_pk_mul_f32 v[136:137], v[128:129], s[6:7] op_sel_hi:[1,0]
	ds_read_b128 v[126:129], v176 offset:23552
	s_waitcnt lgkmcnt(1)
	v_pk_fma_f32 v[74:75], v[74:75], v[94:95], v[136:137]
	v_pk_fma_f32 v[76:77], v[76:77], v[92:93], v[134:135]
	s_waitcnt vmcnt(0)
	v_lshlrev_b32_e32 v134, 16, v162
	v_and_b32_e32 v135, 0xffff0000, v162
	v_lshlrev_b32_e32 v136, 16, v163
	v_and_b32_e32 v137, 0xffff0000, v163
	v_pk_mul_f32 v[134:135], v[134:135], s[6:7] op_sel_hi:[1,0]
	v_pk_mul_f32 v[136:137], v[136:137], s[6:7] op_sel_hi:[1,0]
	s_waitcnt lgkmcnt(0)
; #define LAS __attribute__((address_space(3)))
; __device__ __forceinline__ void phase_combine(const Frame& F, const Args& a, int layer) {
;     ...
;                 f[i] = xv * ALPHA + *(const LAS f32x4*)(pg2 + c) * f[i]; s += (f[i][0] + f[i][1]) + (f[i][2] + f[i][3]); }
;             const float mean = wave_sum(s) * (1.0f / D); float ss = 0.f;
; #pragma unroll
;             for (int i = 0; i < 8; ++i) { f[i] = f[i] - mean; ss += (f[i][0] * f[i][0] + f[i][1] * f[i][1]) + (f[i][2] * f[i][2] + f[i][3] * f[i][3]); }
;             const float rstd = rsqrtf(wave_sum(ss) * (1.0f / D) + LN_EPS);
	v_pk_fma_f32 v[72:73], v[72:73], v[126:127], v[134:135]
	v_pk_fma_f32 v[70:71], v[70:71], v[128:129], v[136:137]
	v_add_f32_e32 v92, v76, v77
	v_add_f32_e32 v94, v74, v75
	v_mov_b32_e32 v131, v72
	v_mov_b32_e32 v133, v73
	v_mov_b32_e32 v93, v70
	v_mov_b32_e32 v95, v71
	v_pk_add_f32 v[126:127], v[130:131], v[132:133]
	v_pk_add_f32 v[92:93], v[92:93], v[94:95]
	s_nop 0
	v_pk_add_f32 v[92:93], v[126:127], v[92:93]
	s_nop 0
	v_add_f32_e32 v92, v92, v93
	s_waitcnt lgkmcnt(0)
	s_nop 1
	v_add_f32_dpp v92, v92, v92 quad_perm:[1,0,3,2] row_mask:0xf bank_mask:0xf
	s_waitcnt lgkmcnt(0)
	s_nop 1
	v_add_f32_dpp v92, v92, v92 quad_perm:[2,3,0,1] row_mask:0xf bank_mask:0xf
	s_waitcnt lgkmcnt(0)
	s_nop 1
	v_add_f32_dpp v92, v92, v92 row_half_mirror row_mask:0xf bank_mask:0xf
	s_waitcnt lgkmcnt(0)
	s_nop 1
	v_add_f32_dpp v92, v92, v92 row_mirror row_mask:0xf bank_mask:0xf
	v_mov_b32_e32 v93, v92
	s_nop 1
	v_permlane16_swap_b32 v93, v92
	s_waitcnt lgkmcnt(0)
	v_add_f32_e32 v92, v92, v93
	v_mov_b32_e32 v93, v92
	s_nop 1
	v_permlane32_swap_b32 v93, v92
	s_waitcnt lgkmcnt(0)
	v_add_f32_e32 v130, v92, v93
	v_fmamk_f32 v105, v130, 0xba000000, v105
	v_fmamk_f32 v99, v130, 0xba000000, v99
	v_fmamk_f32 v103, v130, 0xba000000, v103
	v_fmac_f32_e32 v104, 0xba000000, v130
	v_fmamk_f32 v101, v130, 0xba000000, v101
	v_fmac_f32_e32 v98, 0xba000000, v130
	v_mov_b32_e32 v94, v105
	v_mov_b32_e32 v95, v99
	v_fmac_f32_e32 v102, 0xba000000, v130
	v_fmac_f32_e32 v100, 0xba000000, v130
	v_mov_b32_e32 v92, v104
	v_mov_b32_e32 v93, v98
	v_pk_mul_f32 v[94:95], v[94:95], v[94:95]
	v_mov_b32_e32 v126, v103
	v_mov_b32_e32 v127, v101
	v_pk_fma_f32 v[92:93], v[92:93], v[92:93], v[94:95]
	v_mov_b32_e32 v94, v102
	v_mov_b32_e32 v95, v100
	v_pk_mul_f32 v[126:127], v[126:127], v[126:127]
	v_fmamk_f32 v97, v130, 0xba000000, v97
	v_pk_fma_f32 v[94:95], v[94:95], v[94:95], v[126:127]
	v_fmac_f32_e32 v96, 0xba000000, v130
	v_pk_add_f32 v[92:93], v[92:93], v[94:95]
	v_fmamk_f32 v91, v130, 0xba000000, v91
	v_fmac_f32_e32 v90, 0xba000000, v130
	v_pk_add_f32 v[92:93], v[92:93], v[92:93] op_sel_hi:[0,1]
	v_pk_mul_f32 v[94:95], v[90:91], v[90:91]
	v_pk_mul_f32 v[126:127], v[96:97], v[96:97]
	v_fmac_f32_e32 v88, 0xba000000, v130
	v_pk_mov_b32 v[128:129], v[126:127], v[94:95] op_sel:[1,0]
	v_mov_b32_e32 v127, v95
	v_fmamk_f32 v89, v130, 0xba000000, v89
	v_fmac_f32_e32 v86, 0xba000000, v130
	v_mul_f32_e32 v92, v88, v88
	v_pk_add_f32 v[94:95], v[128:129], v[126:127]
	v_fmamk_f32 v87, v130, 0xba000000, v87
	v_pk_fma_f32 v[126:127], v[88:89], v[88:89], v[92:93] op_sel_hi:[1,1,0]
	v_mul_f32_e32 v92, v86, v86
	v_pk_add_f32 v[94:95], v[94:95], v[94:95] op_sel_hi:[0,1]
	v_pk_fma_f32 v[128:129], v[86:87], v[86:87], v[92:93] op_sel_hi:[1,1,0]
	v_fmamk_f32 v83, v130, 0xba000000, v83
	v_fmac_f32_e32 v82, 0xba000000, v130
	v_fmamk_f32 v85, v130, 0xba000000, v85
	v_fmac_f32_e32 v84, 0xba000000, v130
	v_mul_f32_e32 v126, v84, v84
	v_mul_f32_e32 v128, v85, v85
	v_mul_f32_e32 v94, v82, v82
	v_mul_f32_e32 v92, v83, v83
	v_pk_add_f32 v[126:127], v[126:127], v[128:129]
	v_pk_add_f32 v[92:93], v[94:95], v[92:93]
	v_fmamk_f32 v81, v130, 0xba000000, v81
	v_pk_add_f32 v[92:93], v[126:127], v[92:93]
	v_fmac_f32_e32 v80, 0xba000000, v130
	v_fmamk_f32 v79, v130, 0xba000000, v79
	v_fmac_f32_e32 v78, 0xba000000, v130
	v_pk_add_f32 v[92:93], v[92:93], v[92:93] op_sel_hi:[0,1]
	v_pk_mul_f32 v[94:95], v[78:79], v[78:79]
	v_pk_mul_f32 v[126:127], v[80:81], v[80:81]
	v_fmac_f32_e32 v76, 0xba000000, v130
	v_pk_mov_b32 v[128:129], v[126:127], v[94:95] op_sel:[1,0]
	v_mov_b32_e32 v127, v95
	v_fmamk_f32 v77, v130, 0xba000000, v77
	v_fmac_f32_e32 v74, 0xba000000, v130
	v_mul_f32_e32 v92, v76, v76
	v_pk_add_f32 v[94:95], v[128:129], v[126:127]
	v_fmamk_f32 v75, v130, 0xba000000, v75
	v_pk_fma_f32 v[126:127], v[76:77], v[76:77], v[92:93] op_sel_hi:[1,1,0]
	v_mul_f32_e32 v92, v74, v74
	v_pk_add_f32 v[94:95], v[94:95], v[94:95] op_sel_hi:[0,1]
	v_pk_fma_f32 v[128:129], v[74:75], v[74:75], v[92:93] op_sel_hi:[1,1,0]
	v_fmamk_f32 v71, v130, 0xba000000, v71
	v_fmac_f32_e32 v70, 0xba000000, v130
	v_fmamk_f32 v73, v130, 0xba000000, v73
	v_fmac_f32_e32 v72, 0xba000000, v130
	v_mul_f32_e32 v126, v72, v72
	v_mul_f32_e32 v128, v73, v73
	v_mul_f32_e32 v94, v70, v70
	v_mul_f32_e32 v92, v71, v71
	v_pk_add_f32 v[126:127], v[126:127], v[128:129]
	v_pk_add_f32 v[92:93], v[94:95], v[92:93]
	s_nop 0
	v_pk_add_f32 v[92:93], v[126:127], v[92:93]
	s_nop 0
	v_add_f32_e32 v92, v92, v93
	s_waitcnt lgkmcnt(0)
; #define GAS __attribute__((address_space(1)))
; #define LAS __attribute__((address_space(3)))
; __device__ __forceinline__ unsigned pk2(float lo, float hi) { return f2bf(lo) | (f2bf(hi) << 16); }
; __device__ __forceinline__ unsigned pk4_fp8(float a, float b, float c, float d) { int w = 0; w = __builtin_amdgcn_cvt_pk_fp8_f32(sat8(a), sat8(b), w, false); w = __builtin_amdgcn_cvt_pk_fp8_f32(sat8(c), sat8(d), w, true); return (unsigned)w; }
; __device__ __forceinline__ void phase_combine(const Frame& F, const Args& a, int layer) {
;     ...
;             const float rstd = rsqrtf(wave_sum(ss) * (1.0f / D) + LN_EPS);
;             if (layer == 0) { const LAS float* psc = P + (3 + 3 * r) * D; const LAS float* psh = P + (4 + 3 * r) * D;
; #pragma unroll
;                 for (int i = 0; i < 8; ++i) { const int c = 4 * F.lane + 256 * i;
;                     const f32x4 lat = f[i] * rstd * *(const LAS f32x4*)(P + c) + *(const LAS f32x4*)(P + D + c);
;                     { u32x2 wl; wl.x = pk2(lat[0], lat[1]); wl.y = pk2(lat[2], lat[3]); *(GAS u32x2*)(xr + c) = wl; }
;                     const f32x4 h = lat * *(const LAS f32x4*)(psc + c) + *(const LAS f32x4*)(psh + c);
;                     *(GAS unsigned*)((unsigned char*)A0 + (size_t)row * D + c) = pk4_fp8(h[0], h[1], h[2], h[3]); } }
;             else { float* o = a.out + (size_t)(row - TC) * D;
; #pragma unroll
;                 for (int i = 0; i < 8; ++i) { const int c = 4 * F.lane + 256 * i; *(GAS f32x4*)(o + c) = f[i] * rstd * *(const LAS f32x4*)(P + c) + *(const LAS f32x4*)(P + D + c); } }
	s_nop 1
	v_add_f32_dpp v92, v92, v92 quad_perm:[1,0,3,2] row_mask:0xf bank_mask:0xf
	s_waitcnt lgkmcnt(0)
	s_nop 1
	v_add_f32_dpp v92, v92, v92 quad_perm:[2,3,0,1] row_mask:0xf bank_mask:0xf
	s_waitcnt lgkmcnt(0)
	s_nop 1
	v_add_f32_dpp v92, v92, v92 row_half_mirror row_mask:0xf bank_mask:0xf
	s_waitcnt lgkmcnt(0)
	s_nop 1
	v_add_f32_dpp v92, v92, v92 row_mirror row_mask:0xf bank_mask:0xf
	v_mov_b32_e32 v93, v92
	s_nop 1
	v_permlane16_swap_b32 v93, v92
	s_waitcnt lgkmcnt(0)
	v_add_f32_e32 v92, v92, v93
	v_mov_b32_e32 v93, v92
	s_nop 1
	v_permlane32_swap_b32 v93, v92
	s_waitcnt lgkmcnt(0)
	v_add_f32_e32 v92, v92, v93
	v_fmamk_f32 v92, v92, 0x3a000000, v115
	v_mul_f32_e32 v93, 0x4b800000, v92
	v_cmp_gt_f32_e32 vcc, s16, v92
	s_nop 1
	v_cndmask_b32_e32 v92, v92, v93, vcc
	v_rsq_f32_e32 v92, v92
	s_nop 0
	v_mul_f32_e32 v93, 0x45800000, v92
	v_cndmask_b32_e32 v126, v92, v93, vcc
	v_pk_mul_f32 v[92:93], v[104:105], v[126:127] op_sel_hi:[1,0]
	v_pk_mul_f32 v[94:95], v[102:103], v[126:127] op_sel_hi:[1,0]
	v_pk_fma_f32 v[92:93], v[0:1], v[92:93], v[8:9]
	v_pk_fma_f32 v[94:95], v[2:3], v[94:95], v[10:11]
	global_store_dwordx4 v64, v[92:95], s[8:9]
	v_pk_mul_f32 v[90:91], v[90:91], v[126:127] op_sel_hi:[1,0]
	v_pk_mul_f32 v[86:87], v[86:87], v[126:127] op_sel_hi:[1,0]
	v_pk_mul_f32 v[92:93], v[98:99], v[126:127] op_sel_hi:[1,0]
	v_pk_mul_f32 v[94:95], v[100:101], v[126:127] op_sel_hi:[1,0]
	v_pk_fma_f32 v[92:93], v[4:5], v[92:93], v[12:13]
	v_pk_fma_f32 v[94:95], v[6:7], v[94:95], v[14:15]
	global_store_dwordx4 v64, v[92:95], s[8:9] offset:1024
	v_pk_mul_f32 v[82:83], v[82:83], v[126:127] op_sel_hi:[1,0]
	v_pk_mul_f32 v[78:79], v[78:79], v[126:127] op_sel_hi:[1,0]
	v_pk_mul_f32 v[94:95], v[96:97], v[126:127] op_sel_hi:[1,0]
	v_pk_fma_f32 v[92:93], v[18:19], v[90:91], v[26:27]
	v_pk_fma_f32 v[90:91], v[16:17], v[94:95], v[24:25]
	global_store_dwordx4 v64, v[90:93], s[8:9] offset:2048
	v_pk_mul_f32 v[74:75], v[74:75], v[126:127] op_sel_hi:[1,0]
	v_pk_mul_f32 v[70:71], v[70:71], v[126:127] op_sel_hi:[1,0]
	v_pk_mul_f32 v[90:91], v[88:89], v[126:127] op_sel_hi:[1,0]
	v_pk_fma_f32 v[88:89], v[22:23], v[86:87], v[30:31]
	v_pk_fma_f32 v[86:87], v[20:21], v[90:91], v[28:29]
	global_store_dwordx4 v64, v[86:89], s[8:9] offset:3072
	s_nop 1
	v_pk_mul_f32 v[86:87], v[84:85], v[126:127] op_sel_hi:[1,0]
	v_pk_fma_f32 v[84:85], v[34:35], v[82:83], v[42:43]
	v_pk_fma_f32 v[82:83], v[32:33], v[86:87], v[40:41]
	global_store_dwordx4 v116, v[82:85], s[8:9]
	s_nop 1
	v_pk_mul_f32 v[82:83], v[80:81], v[126:127] op_sel_hi:[1,0]
	v_pk_fma_f32 v[80:81], v[38:39], v[78:79], v[46:47]
	v_pk_fma_f32 v[78:79], v[36:37], v[82:83], v[44:45]
	global_store_dwordx4 v117, v[78:81], s[8:9]
	s_nop 1
	v_pk_mul_f32 v[78:79], v[76:77], v[126:127] op_sel_hi:[1,0]
	v_pk_fma_f32 v[76:77], v[50:51], v[74:75], v[58:59]
	v_pk_fma_f32 v[74:75], v[48:49], v[78:79], v[56:57]
	global_store_dwordx4 v118, v[74:77], s[8:9]
	s_nop 1
	v_pk_mul_f32 v[74:75], v[72:73], v[126:127] op_sel_hi:[1,0]
	v_pk_fma_f32 v[72:73], v[54:55], v[70:71], v[62:63]
	v_pk_fma_f32 v[70:71], v[52:53], v[74:75], v[60:61]
	global_store_dwordx4 v119, v[70:73], s[8:9]
	s_add_i32 s8, s20, 8
	s_cmp_gt_u32 s20, 23
	s_mov_b32 s20, s8
	s_cbranch_scc0 .LBB0_3531
	s_branch .LBB0_3528
